# phase B latency fixes: conv GLU loads hoisted, pool staging loads hoisted + window-sum LDS reads pipelined 4 deep, 16-lane group-norm sums via DPP instead of ds_bpermute
# speedup vs baseline: 1.0031x; 1.0031x over previous
.LBB0_805:
	s_and_b32 s28, s27, 3
	s_or_b32 s2, s28, s23
	s_ashr_i32 s3, s2, 31
	s_and_b32 s29, s25, 0xffffff80
	s_lshl_b64 s[2:3], s[2:3], 15
	v_add_u32_e32 v84, s29, v48
	v_mov_b64_e32 v[36:37], s[12:13]
	v_lshl_add_u64 v[4:5], v[60:61], 0, s[2:3]
	v_mad_i64_i32 v[20:21], s[2:3], v84, s86, v[36:37]
	s_lshl_b32 s46, s28, 8
	v_lshl_add_u64 v[20:21], v[20:21], 0, s[46:47]
	v_mov_b32_e32 v51, v3
	v_lshl_add_u64 v[20:21], v[20:21], 0, v[50:51]
	s_lshl_b32 s2, s28, 2
	s_mov_b32 s3, s47
	v_or_b32_e32 v38, s29, v86
	global_load_dwordx4 v[16:19], v[4:5], off
	global_load_dwordx4 v[12:15], v[4:5], off offset:64
	global_load_dwordx4 v[8:11], v[4:5], off offset:128
	s_nop 0
	global_load_dwordx4 v[4:7], v[4:5], off offset:192
	s_nop 0
	global_load_dwordx2 v[82:83], v[20:21], off
	global_load_dwordx2 v[80:81], v[20:21], off offset:32
	global_load_dwordx2 v[78:79], v[20:21], off offset:64
	global_load_dwordx2 v[76:77], v[20:21], off offset:96
	global_load_dwordx2 v[74:75], v[20:21], off offset:128
	global_load_dwordx2 v[72:73], v[20:21], off offset:160
	global_load_dwordx2 v[70:71], v[20:21], off offset:192
	global_load_dwordx2 v[68:69], v[20:21], off offset:224
	v_lshl_add_u64 v[20:21], v[62:63], 0, s[2:3]
	s_lshl_b32 s2, s28, 9
	v_add_u32_e32 v51, s20, v38
	v_lshl_add_u64 v[24:25], v[64:65], 0, s[2:3]
	v_lshl_add_u64 v[32:33], v[66:67], 0, s[2:3]
	v_mad_i64_i32 v[38:39], s[2:3], v51, s86, v[36:37]
	v_lshl_add_u64 v[38:39], v[38:39], 0, s[46:47]
	v_lshl_add_u64 v[38:39], v[38:39], 0, v[2:3]
	global_load_dword v151, v[20:21], off
	s_nop 0
	global_load_dwordx4 v[20:23], v[24:25], off offset:16
	global_load_dwordx4 v[28:31], v[24:25], off
	s_nop 0
	global_load_dwordx4 v[24:27], v[32:33], off offset:16
	s_nop 0
	global_load_dwordx4 v[32:35], v[32:33], off
	s_nop 0
	global_load_dwordx4 v[158:161], v[38:39], off offset:1024
	v_or_b32_e32 v38, 4, v51
	v_mad_i64_i32 v[38:39], s[2:3], v38, s86, v[36:37]
	v_lshl_add_u64 v[38:39], v[38:39], 0, s[46:47]
	v_lshl_add_u64 v[38:39], v[38:39], 0, v[2:3]
	global_load_dwordx4 v[44:47], v[38:39], off offset:1024
	v_or_b32_e32 v38, 8, v51
	v_mad_i64_i32 v[38:39], s[2:3], v38, s86, v[36:37]
	v_lshl_add_u64 v[38:39], v[38:39], 0, s[46:47]
	v_lshl_add_u64 v[38:39], v[38:39], 0, v[2:3]
	global_load_dwordx4 v[40:43], v[38:39], off offset:1024
	v_or_b32_e32 v38, 12, v51
	v_mad_i64_i32 v[36:37], s[2:3], v38, s86, v[36:37]
	v_lshl_add_u64 v[36:37], v[36:37], 0, s[46:47]
	v_lshl_add_u64 v[36:37], v[36:37], 0, v[2:3]
	global_load_dwordx4 v[36:39], v[36:37], off offset:1024
	s_waitcnt vmcnt(3)
	v_lshlrev_b32_e32 v156, 16, v158
	v_and_b32_e32 v157, 0xffff0000, v158
	v_mul_f32_e32 v158, 0x3d372713, v156
	v_lshlrev_b32_e32 v155, 16, v159
	v_and_b32_e32 v154, 0xffff0000, v159
	v_mul_f32_e32 v158, v158, v156
	v_mul_f32_e32 v159, 0x3d372713, v157
	v_lshlrev_b32_e32 v85, 16, v161
	v_and_b32_e32 v51, 0xffff0000, v161
	v_fma_f32 v158, v158, v156, v156
	v_mul_f32_e32 v159, v159, v157
	v_mul_f32_e32 v161, 0x3d372713, v155
	v_lshlrev_b32_e32 v153, 16, v160
	v_mul_f32_e32 v158, 0x3fcc422a, v158
	v_fma_f32 v159, v159, v157, v157
	v_mul_f32_e32 v161, v161, v155
	v_mul_f32_e32 v162, 0x3d372713, v154
	v_and_b32_e32 v152, 0xffff0000, v160
	v_mul_f32_e32 v158, 0xbfb8aa3b, v158
	v_mul_f32_e32 v159, 0x3fcc422a, v159
	v_fma_f32 v161, v161, v155, v155
	v_mul_f32_e32 v162, v162, v154
	v_mul_f32_e32 v163, 0x3d372713, v153
	v_exp_f32_e32 v158, v158
	v_mul_f32_e32 v159, 0xbfb8aa3b, v159
	v_mul_f32_e32 v161, 0x3fcc422a, v161
	v_fma_f32 v162, v162, v154, v154
	v_mul_f32_e32 v163, v163, v153
	v_mul_f32_e32 v164, 0x3d372713, v152
	v_exp_f32_e32 v159, v159
	v_mul_f32_e32 v161, 0xbfb8aa3b, v161
	v_mul_f32_e32 v162, 0x3fcc422a, v162
	v_fma_f32 v163, v163, v153, v153
	v_mul_f32_e32 v164, v164, v152
	v_mul_f32_e32 v165, 0x3d372713, v85
	v_exp_f32_e32 v161, v161
	v_mul_f32_e32 v162, 0xbfb8aa3b, v162
	v_mul_f32_e32 v163, 0x3fcc422a, v163
	v_fma_f32 v164, v164, v152, v152
	v_mul_f32_e32 v165, v165, v85
	v_mul_f32_e32 v166, 0x3d372713, v51
	v_exp_f32_e32 v162, v162
	v_mul_f32_e32 v163, 0xbfb8aa3b, v163
	v_mul_f32_e32 v164, 0x3fcc422a, v164
	v_fma_f32 v165, v165, v85, v85
	v_mul_f32_e32 v166, v166, v51
	v_add_f32_e32 v158, 1.0, v158
	v_exp_f32_e32 v163, v163
	v_mul_f32_e32 v164, 0xbfb8aa3b, v164
	v_mul_f32_e32 v165, 0x3fcc422a, v165
	v_fma_f32 v166, v166, v51, v51
	v_rcp_f32_e32 v158, v158
	v_add_f32_e32 v159, 1.0, v159
	v_exp_f32_e32 v164, v164
	v_mul_f32_e32 v165, 0xbfb8aa3b, v165
	v_mul_f32_e32 v166, 0x3fcc422a, v166
	v_rcp_f32_e32 v159, v159
	v_add_f32_e32 v161, 1.0, v161
	v_exp_f32_e32 v165, v165
	v_mul_f32_e32 v166, 0xbfb8aa3b, v166
	v_rcp_f32_e32 v161, v161
	v_add_f32_e32 v162, 1.0, v162
	v_exp_f32_e32 v166, v166
	v_rcp_f32_e32 v162, v162
	v_add_f32_e32 v163, 1.0, v163
	v_fma_f32 v160, v158, v156, 0
	v_rcp_f32_e32 v163, v163
	v_add_f32_e32 v164, 1.0, v164
	v_fmac_f32_e32 v160, v159, v157
	v_rcp_f32_e32 v164, v164
	v_add_f32_e32 v165, 1.0, v165
	v_fmac_f32_e32 v160, v161, v155
	v_rcp_f32_e32 v165, v165
	v_add_f32_e32 v166, 1.0, v166
	v_fmac_f32_e32 v160, v162, v154
	v_rcp_f32_e32 v166, v166
	v_fmac_f32_e32 v160, v163, v153
	v_fmac_f32_e32 v160, v164, v152
	v_fmac_f32_e32 v160, v165, v85
	v_fmac_f32_e32 v160, v166, v51
	s_nop 0
	s_waitcnt lgkmcnt(0)
	v_add_f32_dpp v160, v160, v160 quad_perm:[1,0,3,2] row_mask:0xf bank_mask:0xf
	s_nop 0
	s_waitcnt lgkmcnt(0)
	v_add_f32_dpp v160, v160, v160 quad_perm:[2,3,0,1] row_mask:0xf bank_mask:0xf
	s_nop 0
	s_waitcnt lgkmcnt(0)
	v_add_f32_dpp v160, v160, v160 row_half_mirror row_mask:0xf bank_mask:0xf
	s_nop 0
	s_waitcnt lgkmcnt(0)
	v_add_f32_dpp v160, v160, v160 row_mirror row_mask:0xf bank_mask:0xf
	v_mul_f32_e32 v160, 0x3c000000, v160
	v_fma_f32 v157, v159, v157, -v160
	v_fma_f32 v156, v158, v156, -v160
	v_mul_f32_e32 v158, v157, v157
	v_fmac_f32_e32 v158, v156, v156
	v_fma_f32 v155, v161, v155, -v160
	v_fmac_f32_e32 v158, v155, v155
	v_fma_f32 v154, v162, v154, -v160
	v_fmac_f32_e32 v158, v154, v154
	v_fma_f32 v153, v163, v153, -v160
	v_fmac_f32_e32 v158, v153, v153
	v_fma_f32 v152, v164, v152, -v160
	v_fmac_f32_e32 v158, v152, v152
	v_fma_f32 v85, v165, v85, -v160
	v_fmac_f32_e32 v158, v85, v85
	v_fma_f32 v51, v166, v51, -v160
	v_fmac_f32_e32 v158, v51, v51
	s_nop 0
	s_waitcnt lgkmcnt(0)
	v_add_f32_dpp v158, v158, v158 quad_perm:[1,0,3,2] row_mask:0xf bank_mask:0xf
	s_nop 0
	s_waitcnt lgkmcnt(0)
	v_add_f32_dpp v158, v158, v158 quad_perm:[2,3,0,1] row_mask:0xf bank_mask:0xf
	s_nop 0
	s_waitcnt lgkmcnt(0)
	v_add_f32_dpp v158, v158, v158 row_half_mirror row_mask:0xf bank_mask:0xf
	s_nop 0
	s_waitcnt lgkmcnt(0)
	v_add_f32_dpp v158, v158, v158 row_mirror row_mask:0xf bank_mask:0xf
	v_fmamk_f32 v158, v158, 0x3c000000, v217
	v_cmp_gt_f32_e32 vcc, s87, v158
	v_mul_f32_e32 v159, 0x4f800000, v158
	s_nop 0
	v_cndmask_b32_e32 v158, v158, v159, vcc
	v_sqrt_f32_e32 v159, v158
	s_nop 0
	v_add_u32_e32 v160, -1, v159
	v_fma_f32 v161, -v160, v159, v158
	v_cmp_ge_f32_e64 s[2:3], 0, v161
	v_add_u32_e32 v161, 1, v159
	s_nop 0
	v_cndmask_b32_e64 v160, v159, v160, s[2:3]
	v_fma_f32 v159, -v161, v159, v158
	v_cmp_lt_f32_e64 s[2:3], 0, v159
	s_nop 1
	v_cndmask_b32_e64 v159, v160, v161, s[2:3]
	v_mul_f32_e32 v160, 0x37800000, v159
	v_cndmask_b32_e32 v159, v159, v160, vcc
	v_cmp_class_f32_e32 vcc, v158, v218
	s_nop 1
	v_cndmask_b32_e32 v158, v159, v158, vcc
	v_div_scale_f32 v159, s[2:3], v158, v158, 1.0
	v_rcp_f32_e32 v160, v159
	s_nop 0
	v_fma_f32 v161, -v159, v160, 1.0
	v_fmac_f32_e32 v160, v161, v160
	v_div_scale_f32 v161, vcc, 1.0, v158, 1.0
	v_mul_f32_e32 v162, v161, v160
	v_fma_f32 v163, -v159, v162, v161
	v_fmac_f32_e32 v162, v163, v160
	v_fma_f32 v159, -v159, v162, v161
	v_div_fmas_f32 v159, v159, v160, v162
	v_div_fixup_f32 v158, v159, v158, 1.0
	v_mul_f32_e32 v156, v156, v158
	v_fma_f32 v156, v28, v156, v32
	v_mul_f32_e32 v157, v157, v158
	v_mul_f32_e32 v154, v154, v158
	v_fma_f32 v157, v29, v157, v33
	v_cvt_pk_bf16_f32 v156, v156, v157
	v_mul_f32_e32 v155, v155, v158
	v_fma_f32 v154, v31, v154, v35
	v_mul_f32_e32 v152, v152, v158
	ds_write_b16 v143, v156
	ds_write_b16_d16_hi v144, v156
	v_fma_f32 v155, v30, v155, v34
	v_cvt_pk_bf16_f32 v154, v155, v154
	v_mul_f32_e32 v153, v153, v158
	v_fma_f32 v152, v21, v152, v25
	v_mul_f32_e32 v51, v51, v158
	ds_write_b16 v145, v154
	ds_write_b16_d16_hi v146, v154
	v_fma_f32 v153, v20, v153, v24
	v_cvt_pk_bf16_f32 v152, v153, v152
	v_mul_f32_e32 v85, v85, v158
	v_fma_f32 v51, v23, v51, v27
	ds_write_b16 v147, v152
	ds_write_b16_d16_hi v148, v152
	v_fma_f32 v85, v22, v85, v26
	v_cvt_pk_bf16_f32 v51, v85, v51
	ds_write_b16 v149, v51
	ds_write_b16_d16_hi v150, v51
	s_waitcnt vmcnt(2)
	v_lshlrev_b32_e32 v51, 16, v44
	v_and_b32_e32 v44, 0xffff0000, v44
	v_mul_f32_e32 v154, 0x3d372713, v51
	v_lshlrev_b32_e32 v85, 16, v45
	v_mul_f32_e32 v154, v154, v51
	v_mul_f32_e32 v156, 0x3d372713, v44
	v_and_b32_e32 v45, 0xffff0000, v45
	v_fma_f32 v154, v154, v51, v51
	v_mul_f32_e32 v156, v156, v44
	v_mul_f32_e32 v157, 0x3d372713, v85
	v_lshlrev_b32_e32 v152, 16, v46
	v_mul_f32_e32 v154, 0x3fcc422a, v154
	v_fma_f32 v156, v156, v44, v44
	v_mul_f32_e32 v157, v157, v85
	v_mul_f32_e32 v158, 0x3d372713, v45
	v_and_b32_e32 v46, 0xffff0000, v46
	v_mul_f32_e32 v154, 0xbfb8aa3b, v154
	v_mul_f32_e32 v156, 0x3fcc422a, v156
	v_fma_f32 v157, v157, v85, v85
	v_mul_f32_e32 v158, v158, v45
	v_mul_f32_e32 v159, 0x3d372713, v152
	v_lshlrev_b32_e32 v153, 16, v47
	v_exp_f32_e32 v154, v154
	v_mul_f32_e32 v156, 0xbfb8aa3b, v156
	v_mul_f32_e32 v157, 0x3fcc422a, v157
	v_fma_f32 v158, v158, v45, v45
	v_mul_f32_e32 v159, v159, v152
	v_mul_f32_e32 v160, 0x3d372713, v46
	v_and_b32_e32 v47, 0xffff0000, v47
	v_exp_f32_e32 v156, v156
	v_mul_f32_e32 v157, 0xbfb8aa3b, v157
	v_mul_f32_e32 v158, 0x3fcc422a, v158
	v_fma_f32 v159, v159, v152, v152
	v_mul_f32_e32 v160, v160, v46
	v_mul_f32_e32 v161, 0x3d372713, v153
	v_exp_f32_e32 v157, v157
	v_mul_f32_e32 v158, 0xbfb8aa3b, v158
	v_mul_f32_e32 v159, 0x3fcc422a, v159
	v_fma_f32 v160, v160, v46, v46
	v_mul_f32_e32 v161, v161, v153
	v_mul_f32_e32 v162, 0x3d372713, v47
	v_exp_f32_e32 v158, v158
	v_mul_f32_e32 v159, 0xbfb8aa3b, v159
	v_mul_f32_e32 v160, 0x3fcc422a, v160
	v_fma_f32 v161, v161, v153, v153
	v_mul_f32_e32 v162, v162, v47
	v_add_f32_e32 v154, 1.0, v154
	v_exp_f32_e32 v159, v159
	v_mul_f32_e32 v160, 0xbfb8aa3b, v160
	v_mul_f32_e32 v161, 0x3fcc422a, v161
	v_fma_f32 v162, v162, v47, v47
	v_rcp_f32_e32 v154, v154
	v_add_f32_e32 v156, 1.0, v156
	v_exp_f32_e32 v160, v160
	v_mul_f32_e32 v161, 0xbfb8aa3b, v161
	v_mul_f32_e32 v162, 0x3fcc422a, v162
	v_rcp_f32_e32 v156, v156
	v_add_f32_e32 v157, 1.0, v157
	v_exp_f32_e32 v161, v161
	v_mul_f32_e32 v162, 0xbfb8aa3b, v162
	v_rcp_f32_e32 v157, v157
	v_add_f32_e32 v158, 1.0, v158
	v_exp_f32_e32 v162, v162
	v_rcp_f32_e32 v158, v158
	v_add_f32_e32 v159, 1.0, v159
	v_fma_f32 v155, v154, v51, 0
	v_rcp_f32_e32 v159, v159
	v_add_f32_e32 v160, 1.0, v160
	v_fmac_f32_e32 v155, v156, v44
	v_rcp_f32_e32 v160, v160
	v_add_f32_e32 v161, 1.0, v161
	v_fmac_f32_e32 v155, v157, v85
	v_rcp_f32_e32 v161, v161
	v_add_f32_e32 v162, 1.0, v162
	v_fmac_f32_e32 v155, v158, v45
	v_rcp_f32_e32 v162, v162
	v_fmac_f32_e32 v155, v159, v152
	v_fmac_f32_e32 v155, v160, v46
	v_fmac_f32_e32 v155, v161, v153
	v_fmac_f32_e32 v155, v162, v47
	s_nop 0
	s_waitcnt lgkmcnt(0)
	v_add_f32_dpp v155, v155, v155 quad_perm:[1,0,3,2] row_mask:0xf bank_mask:0xf
	s_nop 0
	s_waitcnt lgkmcnt(0)
	v_add_f32_dpp v155, v155, v155 quad_perm:[2,3,0,1] row_mask:0xf bank_mask:0xf
	s_nop 0
	s_waitcnt lgkmcnt(0)
	v_add_f32_dpp v155, v155, v155 row_half_mirror row_mask:0xf bank_mask:0xf
	s_nop 0
	s_waitcnt lgkmcnt(0)
	v_add_f32_dpp v155, v155, v155 row_mirror row_mask:0xf bank_mask:0xf
	v_mul_f32_e32 v155, 0x3c000000, v155
	v_fma_f32 v44, v156, v44, -v155
	v_fma_f32 v51, v154, v51, -v155
	v_mul_f32_e32 v154, v44, v44
	v_fmac_f32_e32 v154, v51, v51
	v_fma_f32 v85, v157, v85, -v155
	v_fmac_f32_e32 v154, v85, v85
	v_fma_f32 v45, v158, v45, -v155
	v_fmac_f32_e32 v154, v45, v45
	v_fma_f32 v152, v159, v152, -v155
	v_fmac_f32_e32 v154, v152, v152
	v_fma_f32 v46, v160, v46, -v155
	v_fmac_f32_e32 v154, v46, v46
	v_fma_f32 v153, v161, v153, -v155
	v_fmac_f32_e32 v154, v153, v153
	v_fma_f32 v47, v162, v47, -v155
	v_fmac_f32_e32 v154, v47, v47
	s_nop 0
	s_waitcnt lgkmcnt(0)
	v_add_f32_dpp v154, v154, v154 quad_perm:[1,0,3,2] row_mask:0xf bank_mask:0xf
	s_nop 0
	s_waitcnt lgkmcnt(0)
	v_add_f32_dpp v154, v154, v154 quad_perm:[2,3,0,1] row_mask:0xf bank_mask:0xf
	s_nop 0
	s_waitcnt lgkmcnt(0)
	v_add_f32_dpp v154, v154, v154 row_half_mirror row_mask:0xf bank_mask:0xf
	s_nop 0
	s_waitcnt lgkmcnt(0)
	v_add_f32_dpp v154, v154, v154 row_mirror row_mask:0xf bank_mask:0xf
	v_fmamk_f32 v154, v154, 0x3c000000, v217
	v_cmp_gt_f32_e32 vcc, s87, v154
	v_mul_f32_e32 v155, 0x4f800000, v154
	s_nop 0
	v_cndmask_b32_e32 v154, v154, v155, vcc
	v_sqrt_f32_e32 v155, v154
	s_nop 0
	v_add_u32_e32 v156, -1, v155
	v_fma_f32 v157, -v156, v155, v154
	v_cmp_ge_f32_e64 s[2:3], 0, v157
	v_add_u32_e32 v157, 1, v155
	s_nop 0
	v_cndmask_b32_e64 v156, v155, v156, s[2:3]
	v_fma_f32 v155, -v157, v155, v154
	v_cmp_lt_f32_e64 s[2:3], 0, v155
	s_nop 1
	v_cndmask_b32_e64 v155, v156, v157, s[2:3]
	v_mul_f32_e32 v156, 0x37800000, v155
	v_cndmask_b32_e32 v155, v155, v156, vcc
	v_cmp_class_f32_e32 vcc, v154, v218
	s_nop 1
	v_cndmask_b32_e32 v154, v155, v154, vcc
	v_div_scale_f32 v155, s[2:3], v154, v154, 1.0
	v_rcp_f32_e32 v156, v155
	s_nop 0
	v_fma_f32 v157, -v155, v156, 1.0
	v_fmac_f32_e32 v156, v157, v156
	v_div_scale_f32 v157, vcc, 1.0, v154, 1.0
	v_mul_f32_e32 v158, v157, v156
	v_fma_f32 v159, -v155, v158, v157
	v_fmac_f32_e32 v158, v159, v156
	v_fma_f32 v155, -v155, v158, v157
	v_div_fmas_f32 v155, v155, v156, v158
	v_div_fixup_f32 v154, v155, v154, 1.0
	v_mul_f32_e32 v44, v44, v154
	v_mul_f32_e32 v51, v51, v154
	v_fma_f32 v44, v29, v44, v33
	v_fma_f32 v51, v28, v51, v32
	v_cvt_pk_bf16_f32 v44, v51, v44
	ds_write_b16 v143, v44 offset:8
	ds_write_b16_d16_hi v144, v44 offset:8
	v_mul_f32_e32 v44, v85, v154
	v_fma_f32 v44, v30, v44, v34
	v_mul_f32_e32 v45, v45, v154
	v_fma_f32 v45, v31, v45, v35
	v_cvt_pk_bf16_f32 v44, v44, v45
	ds_write_b16 v145, v44 offset:8
	ds_write_b16_d16_hi v146, v44 offset:8
	v_mul_f32_e32 v44, v152, v154
	v_fma_f32 v44, v20, v44, v24
	v_mul_f32_e32 v45, v46, v154
	v_fma_f32 v45, v21, v45, v25
	v_cvt_pk_bf16_f32 v44, v44, v45
	ds_write_b16 v147, v44 offset:8
	ds_write_b16_d16_hi v148, v44 offset:8
	v_mul_f32_e32 v44, v153, v154
	v_fma_f32 v44, v22, v44, v26
	v_mul_f32_e32 v45, v47, v154
	v_fma_f32 v45, v23, v45, v27
	v_cvt_pk_bf16_f32 v44, v44, v45
	ds_write_b16 v149, v44 offset:8
	ds_write_b16_d16_hi v150, v44 offset:8
	s_waitcnt vmcnt(1)
	v_lshlrev_b32_e32 v44, 16, v40
	v_and_b32_e32 v40, 0xffff0000, v40
	v_mul_f32_e32 v51, 0x3d372713, v44
	v_lshlrev_b32_e32 v45, 16, v41
	v_mul_f32_e32 v51, v51, v44
	v_mul_f32_e32 v152, 0x3d372713, v40
	v_and_b32_e32 v41, 0xffff0000, v41
	v_fma_f32 v51, v51, v44, v44
	v_mul_f32_e32 v152, v152, v40
	v_mul_f32_e32 v153, 0x3d372713, v45
	v_lshlrev_b32_e32 v46, 16, v42
	v_mul_f32_e32 v51, 0x3fcc422a, v51
	v_fma_f32 v152, v152, v40, v40
	v_mul_f32_e32 v153, v153, v45
	v_mul_f32_e32 v154, 0x3d372713, v41
	v_and_b32_e32 v42, 0xffff0000, v42
	v_mul_f32_e32 v51, 0xbfb8aa3b, v51
	v_mul_f32_e32 v152, 0x3fcc422a, v152
	v_fma_f32 v153, v153, v45, v45
	v_mul_f32_e32 v154, v154, v41
	v_mul_f32_e32 v155, 0x3d372713, v46
	v_lshlrev_b32_e32 v47, 16, v43
	v_exp_f32_e32 v51, v51
	v_mul_f32_e32 v152, 0xbfb8aa3b, v152
	v_mul_f32_e32 v153, 0x3fcc422a, v153
	v_fma_f32 v154, v154, v41, v41
	v_mul_f32_e32 v155, v155, v46
	v_mul_f32_e32 v156, 0x3d372713, v42
	v_and_b32_e32 v43, 0xffff0000, v43
	v_exp_f32_e32 v152, v152
	v_mul_f32_e32 v153, 0xbfb8aa3b, v153
	v_mul_f32_e32 v154, 0x3fcc422a, v154
	v_fma_f32 v155, v155, v46, v46
	v_mul_f32_e32 v156, v156, v42
	v_mul_f32_e32 v157, 0x3d372713, v47
	v_exp_f32_e32 v153, v153
	v_mul_f32_e32 v154, 0xbfb8aa3b, v154
	v_mul_f32_e32 v155, 0x3fcc422a, v155
	v_fma_f32 v156, v156, v42, v42
	v_mul_f32_e32 v157, v157, v47
	v_mul_f32_e32 v158, 0x3d372713, v43
	v_exp_f32_e32 v154, v154
	v_mul_f32_e32 v155, 0xbfb8aa3b, v155
	v_mul_f32_e32 v156, 0x3fcc422a, v156
	v_fma_f32 v157, v157, v47, v47
	v_mul_f32_e32 v158, v158, v43
	v_add_f32_e32 v51, 1.0, v51
	v_exp_f32_e32 v155, v155
	v_mul_f32_e32 v156, 0xbfb8aa3b, v156
	v_mul_f32_e32 v157, 0x3fcc422a, v157
	v_fma_f32 v158, v158, v43, v43
	v_rcp_f32_e32 v51, v51
	v_add_f32_e32 v152, 1.0, v152
	v_exp_f32_e32 v156, v156
	v_mul_f32_e32 v157, 0xbfb8aa3b, v157
	v_mul_f32_e32 v158, 0x3fcc422a, v158
	v_rcp_f32_e32 v152, v152
	v_add_f32_e32 v153, 1.0, v153
	v_exp_f32_e32 v157, v157
	v_mul_f32_e32 v158, 0xbfb8aa3b, v158
	v_rcp_f32_e32 v153, v153
	v_add_f32_e32 v154, 1.0, v154
	v_exp_f32_e32 v158, v158
	v_rcp_f32_e32 v154, v154
	v_add_f32_e32 v155, 1.0, v155
	v_fma_f32 v85, v51, v44, 0
	v_rcp_f32_e32 v155, v155
	v_add_f32_e32 v156, 1.0, v156
	v_fmac_f32_e32 v85, v152, v40
	v_rcp_f32_e32 v156, v156
	v_add_f32_e32 v157, 1.0, v157
	v_fmac_f32_e32 v85, v153, v45
	v_rcp_f32_e32 v157, v157
	v_add_f32_e32 v158, 1.0, v158
	v_fmac_f32_e32 v85, v154, v41
	v_rcp_f32_e32 v158, v158
	v_fmac_f32_e32 v85, v155, v46
	v_fmac_f32_e32 v85, v156, v42
	v_fmac_f32_e32 v85, v157, v47
	v_fmac_f32_e32 v85, v158, v43
	s_nop 0
	s_waitcnt lgkmcnt(0)
	v_add_f32_dpp v85, v85, v85 quad_perm:[1,0,3,2] row_mask:0xf bank_mask:0xf
	s_nop 0
	s_waitcnt lgkmcnt(0)
	v_add_f32_dpp v85, v85, v85 quad_perm:[2,3,0,1] row_mask:0xf bank_mask:0xf
	s_nop 0
	s_waitcnt lgkmcnt(0)
	v_add_f32_dpp v85, v85, v85 row_half_mirror row_mask:0xf bank_mask:0xf
	s_nop 0
	s_waitcnt lgkmcnt(0)
	v_add_f32_dpp v85, v85, v85 row_mirror row_mask:0xf bank_mask:0xf
	v_mul_f32_e32 v85, 0x3c000000, v85
	v_fma_f32 v40, v152, v40, -v85
	v_fma_f32 v44, v51, v44, -v85
	v_mul_f32_e32 v51, v40, v40
	v_fmac_f32_e32 v51, v44, v44
	v_fma_f32 v45, v153, v45, -v85
	v_fmac_f32_e32 v51, v45, v45
	v_fma_f32 v41, v154, v41, -v85
	v_fmac_f32_e32 v51, v41, v41
	v_fma_f32 v46, v155, v46, -v85
	v_fmac_f32_e32 v51, v46, v46
	v_fma_f32 v42, v156, v42, -v85
	v_fmac_f32_e32 v51, v42, v42
	v_fma_f32 v47, v157, v47, -v85
	v_fmac_f32_e32 v51, v47, v47
	v_fma_f32 v43, v158, v43, -v85
	v_fmac_f32_e32 v51, v43, v43
	s_nop 0
	s_waitcnt lgkmcnt(0)
	v_add_f32_dpp v51, v51, v51 quad_perm:[1,0,3,2] row_mask:0xf bank_mask:0xf
	s_nop 0
	s_waitcnt lgkmcnt(0)
	v_add_f32_dpp v51, v51, v51 quad_perm:[2,3,0,1] row_mask:0xf bank_mask:0xf
	s_nop 0
	s_waitcnt lgkmcnt(0)
	v_add_f32_dpp v51, v51, v51 row_half_mirror row_mask:0xf bank_mask:0xf
	s_nop 0
	s_waitcnt lgkmcnt(0)
	v_add_f32_dpp v51, v51, v51 row_mirror row_mask:0xf bank_mask:0xf
	v_fmamk_f32 v51, v51, 0x3c000000, v217
	v_cmp_gt_f32_e32 vcc, s87, v51
	v_mul_f32_e32 v85, 0x4f800000, v51
	s_nop 0
	v_cndmask_b32_e32 v51, v51, v85, vcc
	v_sqrt_f32_e32 v85, v51
	s_nop 0
	v_add_u32_e32 v152, -1, v85
	v_fma_f32 v153, -v152, v85, v51
	v_cmp_ge_f32_e64 s[2:3], 0, v153
	v_add_u32_e32 v153, 1, v85
	s_nop 0
	v_cndmask_b32_e64 v152, v85, v152, s[2:3]
	v_fma_f32 v85, -v153, v85, v51
	v_cmp_lt_f32_e64 s[2:3], 0, v85
	s_nop 1
	v_cndmask_b32_e64 v85, v152, v153, s[2:3]
	v_mul_f32_e32 v152, 0x37800000, v85
	v_cndmask_b32_e32 v85, v85, v152, vcc
	v_cmp_class_f32_e32 vcc, v51, v218
	s_nop 1
	v_cndmask_b32_e32 v51, v85, v51, vcc
	v_div_scale_f32 v85, s[2:3], v51, v51, 1.0
	v_rcp_f32_e32 v152, v85
	s_nop 0
	v_fma_f32 v153, -v85, v152, 1.0
	v_fmac_f32_e32 v152, v153, v152
	v_div_scale_f32 v153, vcc, 1.0, v51, 1.0
	v_mul_f32_e32 v154, v153, v152
	v_fma_f32 v155, -v85, v154, v153
	v_fmac_f32_e32 v154, v155, v152
	v_fma_f32 v85, -v85, v154, v153
	v_div_fmas_f32 v85, v85, v152, v154
	v_div_fixup_f32 v51, v85, v51, 1.0
	v_mul_f32_e32 v40, v40, v51
	v_mul_f32_e32 v44, v44, v51
	v_fma_f32 v40, v29, v40, v33
	v_fma_f32 v44, v28, v44, v32
	v_cvt_pk_bf16_f32 v40, v44, v40
	ds_write_b16 v55, v40
	ds_write_b16_d16_hi v59, v40
	v_mul_f32_e32 v40, v45, v51
	v_fma_f32 v40, v30, v40, v34
	v_mul_f32_e32 v41, v41, v51
	v_fma_f32 v41, v31, v41, v35
	v_cvt_pk_bf16_f32 v40, v40, v41
	ds_write_b16 v89, v40
	ds_write_b16_d16_hi v90, v40
	v_mul_f32_e32 v40, v46, v51
	v_fma_f32 v40, v20, v40, v24
	v_mul_f32_e32 v41, v42, v51
	v_fma_f32 v41, v21, v41, v25
	v_cvt_pk_bf16_f32 v40, v40, v41
	ds_write_b16 v91, v40
	ds_write_b16_d16_hi v92, v40
	v_mul_f32_e32 v40, v47, v51
	v_fma_f32 v40, v22, v40, v26
	v_mul_f32_e32 v41, v43, v51
	v_fma_f32 v41, v23, v41, v27
	v_cvt_pk_bf16_f32 v40, v40, v41
	ds_write_b16 v93, v40
	ds_write_b16_d16_hi v94, v40
	s_waitcnt vmcnt(0)
	v_lshlrev_b32_e32 v40, 16, v36
	v_and_b32_e32 v36, 0xffff0000, v36
	v_mul_f32_e32 v44, 0x3d372713, v40
	v_lshlrev_b32_e32 v41, 16, v37
	v_mul_f32_e32 v44, v44, v40
	v_mul_f32_e32 v46, 0x3d372713, v36
	v_and_b32_e32 v37, 0xffff0000, v37
	v_fma_f32 v44, v44, v40, v40
	v_mul_f32_e32 v46, v46, v36
	v_mul_f32_e32 v47, 0x3d372713, v41
	v_lshlrev_b32_e32 v42, 16, v38
	v_mul_f32_e32 v44, 0x3fcc422a, v44
	v_fma_f32 v46, v46, v36, v36
	v_mul_f32_e32 v47, v47, v41
	v_mul_f32_e32 v51, 0x3d372713, v37
	v_and_b32_e32 v38, 0xffff0000, v38
	v_mul_f32_e32 v44, 0xbfb8aa3b, v44
	v_mul_f32_e32 v46, 0x3fcc422a, v46
	v_fma_f32 v47, v47, v41, v41
	v_mul_f32_e32 v51, v51, v37
	v_mul_f32_e32 v85, 0x3d372713, v42
	v_lshlrev_b32_e32 v43, 16, v39
	v_exp_f32_e32 v44, v44
	v_mul_f32_e32 v46, 0xbfb8aa3b, v46
	v_mul_f32_e32 v47, 0x3fcc422a, v47
	v_fma_f32 v51, v51, v37, v37
	v_mul_f32_e32 v85, v85, v42
	v_mul_f32_e32 v152, 0x3d372713, v38
	v_and_b32_e32 v39, 0xffff0000, v39
	v_exp_f32_e32 v46, v46
	v_mul_f32_e32 v47, 0xbfb8aa3b, v47
	v_mul_f32_e32 v51, 0x3fcc422a, v51
	v_fma_f32 v85, v85, v42, v42
	v_mul_f32_e32 v152, v152, v38
	v_mul_f32_e32 v153, 0x3d372713, v43
	v_exp_f32_e32 v47, v47
	v_mul_f32_e32 v51, 0xbfb8aa3b, v51
	v_mul_f32_e32 v85, 0x3fcc422a, v85
	v_fma_f32 v152, v152, v38, v38
	v_mul_f32_e32 v153, v153, v43
	v_mul_f32_e32 v154, 0x3d372713, v39
	v_exp_f32_e32 v51, v51
	v_mul_f32_e32 v85, 0xbfb8aa3b, v85
	v_mul_f32_e32 v152, 0x3fcc422a, v152
	v_fma_f32 v153, v153, v43, v43
	v_mul_f32_e32 v154, v154, v39
	v_add_f32_e32 v44, 1.0, v44
	v_exp_f32_e32 v85, v85
	v_mul_f32_e32 v152, 0xbfb8aa3b, v152
	v_mul_f32_e32 v153, 0x3fcc422a, v153
	v_fma_f32 v154, v154, v39, v39
	v_rcp_f32_e32 v44, v44
	v_add_f32_e32 v46, 1.0, v46
	v_exp_f32_e32 v152, v152
	v_mul_f32_e32 v153, 0xbfb8aa3b, v153
	v_mul_f32_e32 v154, 0x3fcc422a, v154
	v_rcp_f32_e32 v46, v46
	v_add_f32_e32 v47, 1.0, v47
	v_exp_f32_e32 v153, v153
	v_mul_f32_e32 v154, 0xbfb8aa3b, v154
	v_rcp_f32_e32 v47, v47
	v_add_f32_e32 v51, 1.0, v51
	v_exp_f32_e32 v154, v154
	v_rcp_f32_e32 v51, v51
	v_add_f32_e32 v85, 1.0, v85
	v_fma_f32 v45, v44, v40, 0
	v_rcp_f32_e32 v85, v85
	v_add_f32_e32 v152, 1.0, v152
	v_fmac_f32_e32 v45, v46, v36
	v_rcp_f32_e32 v152, v152
	v_add_f32_e32 v153, 1.0, v153
	v_fmac_f32_e32 v45, v47, v41
	v_rcp_f32_e32 v153, v153
	v_add_f32_e32 v154, 1.0, v154
	v_fmac_f32_e32 v45, v51, v37
	v_rcp_f32_e32 v154, v154
	v_fmac_f32_e32 v45, v85, v42
	v_fmac_f32_e32 v45, v152, v38
	v_fmac_f32_e32 v45, v153, v43
	v_fmac_f32_e32 v45, v154, v39
	s_nop 0
	s_waitcnt lgkmcnt(0)
	v_add_f32_dpp v45, v45, v45 quad_perm:[1,0,3,2] row_mask:0xf bank_mask:0xf
	s_nop 0
	s_waitcnt lgkmcnt(0)
	v_add_f32_dpp v45, v45, v45 quad_perm:[2,3,0,1] row_mask:0xf bank_mask:0xf
	s_nop 0
	s_waitcnt lgkmcnt(0)
	v_add_f32_dpp v45, v45, v45 row_half_mirror row_mask:0xf bank_mask:0xf
	s_nop 0
	s_waitcnt lgkmcnt(0)
	v_add_f32_dpp v45, v45, v45 row_mirror row_mask:0xf bank_mask:0xf
	v_mul_f32_e32 v45, 0x3c000000, v45
	v_fma_f32 v36, v46, v36, -v45
	v_fma_f32 v40, v44, v40, -v45
	v_mul_f32_e32 v44, v36, v36
	v_fmac_f32_e32 v44, v40, v40
	v_fma_f32 v41, v47, v41, -v45
	v_fmac_f32_e32 v44, v41, v41
	v_fma_f32 v37, v51, v37, -v45
	v_fmac_f32_e32 v44, v37, v37
	v_fma_f32 v42, v85, v42, -v45
	v_fmac_f32_e32 v44, v42, v42
	v_fma_f32 v38, v152, v38, -v45
	v_fmac_f32_e32 v44, v38, v38
	v_fma_f32 v43, v153, v43, -v45
	v_fmac_f32_e32 v44, v43, v43
	v_fma_f32 v39, v154, v39, -v45
	v_fmac_f32_e32 v44, v39, v39
	s_nop 0
	s_waitcnt lgkmcnt(0)
	v_add_f32_dpp v44, v44, v44 quad_perm:[1,0,3,2] row_mask:0xf bank_mask:0xf
	s_nop 0
	s_waitcnt lgkmcnt(0)
	v_add_f32_dpp v44, v44, v44 quad_perm:[2,3,0,1] row_mask:0xf bank_mask:0xf
	s_nop 0
	s_waitcnt lgkmcnt(0)
	v_add_f32_dpp v44, v44, v44 row_half_mirror row_mask:0xf bank_mask:0xf
	s_nop 0
	s_waitcnt lgkmcnt(0)
	v_add_f32_dpp v44, v44, v44 row_mirror row_mask:0xf bank_mask:0xf
	v_fmamk_f32 v44, v44, 0x3c000000, v217
	v_cmp_gt_f32_e32 vcc, s87, v44
	v_mul_f32_e32 v45, 0x4f800000, v44
	s_nop 0
	v_cndmask_b32_e32 v44, v44, v45, vcc
	v_sqrt_f32_e32 v45, v44
	s_nop 0
	v_add_u32_e32 v46, -1, v45
	v_fma_f32 v47, -v46, v45, v44
	v_cmp_ge_f32_e64 s[2:3], 0, v47
	v_add_u32_e32 v47, 1, v45
	s_nop 0
	v_cndmask_b32_e64 v46, v45, v46, s[2:3]
	v_fma_f32 v45, -v47, v45, v44
	v_cmp_lt_f32_e64 s[2:3], 0, v45
	s_nop 1
	v_cndmask_b32_e64 v45, v46, v47, s[2:3]
	v_mul_f32_e32 v46, 0x37800000, v45
	v_cndmask_b32_e32 v45, v45, v46, vcc
	v_cmp_class_f32_e32 vcc, v44, v218
	s_nop 1
	v_cndmask_b32_e32 v44, v45, v44, vcc
	v_div_scale_f32 v45, s[2:3], v44, v44, 1.0
	v_rcp_f32_e32 v46, v45
	s_nop 0
	v_fma_f32 v47, -v45, v46, 1.0
	v_fmac_f32_e32 v46, v47, v46
	v_div_scale_f32 v47, vcc, 1.0, v44, 1.0
	v_mul_f32_e32 v51, v47, v46
	v_fma_f32 v85, -v45, v51, v47
	v_fmac_f32_e32 v51, v85, v46
	v_fma_f32 v45, -v45, v51, v47
	v_div_fmas_f32 v45, v45, v46, v51
	v_div_fixup_f32 v44, v45, v44, 1.0
	v_mul_f32_e32 v40, v40, v44
	v_fma_f32 v28, v28, v40, v32
	v_mul_f32_e32 v32, v36, v44
	v_fma_f32 v29, v29, v32, v33
	v_cvt_pk_bf16_f32 v28, v28, v29
	ds_write_b16 v95, v28
	ds_write_b16_d16_hi v96, v28
	v_mul_f32_e32 v28, v41, v44
	v_fma_f32 v28, v30, v28, v34
	v_mul_f32_e32 v29, v37, v44
	v_fmac_f32_e32 v35, v31, v29
	v_cvt_pk_bf16_f32 v28, v28, v35
	ds_write_b16 v97, v28
	ds_write_b16_d16_hi v98, v28
	v_mul_f32_e32 v28, v42, v44
	v_fma_f32 v20, v20, v28, v24
	v_mul_f32_e32 v24, v38, v44
	v_fma_f32 v21, v21, v24, v25
	v_cvt_pk_bf16_f32 v20, v20, v21
	ds_write_b16 v107, v20
	ds_write_b16_d16_hi v108, v20
	v_mul_f32_e32 v20, v43, v44
	v_fma_f32 v20, v22, v20, v26
	v_mul_f32_e32 v21, v39, v44
	v_fmac_f32_e32 v27, v23, v21
	v_cvt_pk_bf16_f32 v20, v20, v27
	s_andn2_b64 vcc, exec, s[4:5]
	ds_write_b16 v109, v20
	ds_write_b16_d16_hi v110, v20
	s_waitcnt lgkmcnt(0)
	s_barrier
	s_cbranch_vccnz .LBB0_807
	ds_read_b128 v[20:23], v111
	ds_read_b128 v[24:27], v112
	s_waitcnt lgkmcnt(1)
	v_mfma_f32_16x16x32_bf16 v[44:47], v[20:23], v[16:19], 0
	ds_read_b128 v[20:23], v113
	ds_read_b128 v[152:155], v118
	s_waitcnt lgkmcnt(2)
	v_mfma_f32_16x16x32_bf16 v[40:43], v[24:27], v[16:19], 0
	ds_read_b128 v[24:27], v114
	s_waitcnt lgkmcnt(2)
	v_mfma_f32_16x16x32_bf16 v[36:39], v[20:23], v[16:19], 0
	ds_read_b128 v[20:23], v115
	s_waitcnt lgkmcnt(1)
	v_mfma_f32_16x16x32_bf16 v[32:35], v[24:27], v[16:19], 0
	ds_read_b128 v[24:27], v116
	s_waitcnt lgkmcnt(1)
	v_mfma_f32_16x16x32_bf16 v[28:31], v[20:23], v[16:19], 0
	ds_read_b128 v[20:23], v117
	s_waitcnt lgkmcnt(1)
	v_mfma_f32_16x16x32_bf16 v[24:27], v[24:27], v[16:19], 0
	s_waitcnt lgkmcnt(0)
	v_mfma_f32_16x16x32_bf16 v[20:23], v[20:23], v[16:19], 0
	v_mfma_f32_16x16x32_bf16 v[16:19], v[152:155], v[16:19], 0
	s_andn2_b64 vcc, exec, s[14:15]
	s_cbranch_vccz .LBB0_808
	s_branch .LBB0_809

.LBB0_815:
	s_and_b32 s28, s26, 3
	s_or_b32 s14, s28, s23
	s_ashr_i32 s15, s14, 31
	s_lshl_b64 s[14:15], s[14:15], 15
	s_add_u32 s14, s24, s14
	s_addc_u32 s15, s25, s15
	v_lshl_add_u64 v[4:5], s[14:15], 0, v[42:43]
	v_lshl_add_u64 v[8:9], s[14:15], 0, v[64:65]
	v_lshl_add_u64 v[12:13], s[14:15], 0, v[66:67]
	v_lshl_add_u64 v[16:17], s[14:15], 0, v[68:69]
	global_load_dwordx4 v[4:7], v[4:5], off
	s_nop 0
	global_load_dwordx4 v[8:11], v[8:9], off
	s_nop 0
	global_load_dwordx4 v[12:15], v[12:13], off
	s_nop 0
	global_load_dwordx4 v[16:19], v[16:17], off
	s_and_saveexec_b64 s[14:15], s[2:3]
	s_xor_b64 s[14:15], exec, s[14:15]
	s_lshl_b32 s46, s28, 7
	s_or_saveexec_b64 s[14:15], s[14:15]
	s_lshl_b32 s16, s26, 5
	s_and_b32 s27, s16, 0xffffff80
	s_and_b32 s29, s16, 0x780
	v_mov_b64_e32 v[56:57], s[46:47]
	s_xor_b64 exec, exec, s[14:15]
	s_cbranch_execz .LBB0_823
	s_sub_i32 s30, 15, s29
	s_add_i32 s31, s27, -16
	s_lshl_b32 s16, s28, 7
	s_mov_b32 s17, s47
	s_mov_b64 s[18:19], 0
	v_ashrrev_i32_e32 v25, 4, v54
	v_add_u32_e32 v22, s31, v25
	v_mov_b64_e32 v[226:227], s[6:7]
	v_mad_i64_i32 v[226:227], s[34:35], v22, s86, v[226:227]
	s_lshl_b32 s46, s16, 1
	v_lshl_add_u64 v[226:227], v[226:227], 0, s[46:47]
	v_lshl_add_u64 v[226:227], v[226:227], 0, v[2:3]
	v_add_co_u32_e32 v226, vcc, 0x3de00000, v226
	s_nop 1
	v_addc_co_u32_e32 v227, vcc, 0, v227, vcc
	v_mad_u64_u32 v[26:27], s[20:21], v25, s1, v[70:71]
	s_movk_i32 s99, 0x100
	v_mov_b32_e32 v20, 0
	v_mov_b32_e32 v21, 0
	v_mov_b32_e32 v22, 0
	v_mov_b32_e32 v23, 0
	v_cmp_lt_i32_e32 vcc, s30, v25
	s_and_saveexec_b64 s[20:21], vcc
	global_load_dwordx4 v[20:23], v[226:227], off offset:2048
	s_mov_b64 exec, s[20:21]
	v_add_co_u32_e32 v226, vcc, 0x30000, v226
	s_nop 1
	v_addc_co_u32_e32 v227, vcc, 0, v227, vcc
	v_mov_b32_e32 v188, 0
	v_mov_b32_e32 v189, 0
	v_mov_b32_e32 v190, 0
	v_mov_b32_e32 v191, 0
	s_sub_i32 s98, s30, 32
	v_cmp_lt_i32_e32 vcc, s98, v25
	s_and_saveexec_b64 s[20:21], vcc
	global_load_dwordx4 v[188:191], v[226:227], off offset:2048
	s_mov_b64 exec, s[20:21]
	v_add_co_u32_e32 v226, vcc, 0x30000, v226
	s_nop 1
	v_addc_co_u32_e32 v227, vcc, 0, v227, vcc
	v_mov_b32_e32 v192, 0
	v_mov_b32_e32 v193, 0
	v_mov_b32_e32 v194, 0
	v_mov_b32_e32 v195, 0
	s_sub_i32 s98, s30, 64
	v_cmp_lt_i32_e32 vcc, s98, v25
	s_and_saveexec_b64 s[20:21], vcc
	global_load_dwordx4 v[192:195], v[226:227], off offset:2048
	s_mov_b64 exec, s[20:21]
	v_add_co_u32_e32 v226, vcc, 0x30000, v226
	s_nop 1
	v_addc_co_u32_e32 v227, vcc, 0, v227, vcc
	v_mov_b32_e32 v204, 0
	v_mov_b32_e32 v205, 0
	v_mov_b32_e32 v206, 0
	v_mov_b32_e32 v207, 0
	s_sub_i32 s98, s30, 96
	v_cmp_lt_i32_e32 vcc, s98, v25
	s_and_saveexec_b64 s[20:21], vcc
	global_load_dwordx4 v[204:207], v[226:227], off offset:2048
	s_mov_b64 exec, s[20:21]
	v_add_co_u32_e32 v226, vcc, 0x30000, v226
	s_nop 1
	v_addc_co_u32_e32 v227, vcc, 0, v227, vcc
	v_mov_b32_e32 v208, 0
	v_mov_b32_e32 v209, 0
	v_mov_b32_e32 v210, 0
	v_mov_b32_e32 v211, 0
	s_sub_i32 s98, s30, 128
	v_cmp_lt_i32_e32 vcc, s98, v25
	v_cmp_gt_i32_e64 s[20:21], s99, v54
	s_nop 1
	s_and_b64 vcc, vcc, s[20:21]
	s_and_saveexec_b64 s[20:21], vcc
	global_load_dwordx4 v[208:211], v[226:227], off offset:2048
	s_mov_b64 exec, s[20:21]
	s_waitcnt vmcnt(4)
	ds_write_b128 v26, v[20:23]
	s_waitcnt vmcnt(3)
	ds_write_b128 v26, v[188:191] offset:8704
	s_waitcnt vmcnt(2)
	ds_write_b128 v26, v[192:195] offset:17408
	s_waitcnt vmcnt(1)
	ds_write_b128 v26, v[204:207] offset:26112
	s_waitcnt vmcnt(0)
	v_cmp_gt_i32_e32 vcc, s99, v54
	s_and_saveexec_b64 s[20:21], vcc
	ds_write_b128 v26, v[208:211] offset:34816
	s_mov_b64 exec, s[20:21]

.LBB0_826:
	s_cmp_lt_u32 s20, 4
	s_cbranch_scc1 .Lmy_pool_t2
	ds_read_b128 v[112:115], v93
	ds_read_b128 v[188:191], v93 offset:272
	ds_read_b128 v[192:195], v93 offset:544
	ds_read_b128 v[204:207], v93 offset:816
	s_add_i32 s20, s20, -4
	v_add_u32_e32 v93, 0x440, v93
	s_waitcnt lgkmcnt(3)
	v_lshlrev_b32_e32 v86, 16, v112
	v_and_b32_e32 v87, 0xffff0000, v112
	v_lshlrev_b32_e32 v84, 16, v113
	v_and_b32_e32 v85, 0xffff0000, v113
	v_lshlrev_b32_e32 v82, 16, v114
	v_and_b32_e32 v83, 0xffff0000, v114
	v_lshlrev_b32_e32 v80, 16, v115
	v_and_b32_e32 v81, 0xffff0000, v115
	v_pk_add_f32 v[74:75], v[74:75], v[86:87]
	v_pk_add_f32 v[78:79], v[78:79], v[84:85]
	v_pk_add_f32 v[76:77], v[76:77], v[82:83]
	v_pk_add_f32 v[72:73], v[72:73], v[80:81]
	s_waitcnt lgkmcnt(2)
	v_lshlrev_b32_e32 v86, 16, v188
	v_and_b32_e32 v87, 0xffff0000, v188
	v_lshlrev_b32_e32 v84, 16, v189
	v_and_b32_e32 v85, 0xffff0000, v189
	v_lshlrev_b32_e32 v82, 16, v190
	v_and_b32_e32 v83, 0xffff0000, v190
	v_lshlrev_b32_e32 v80, 16, v191
	v_and_b32_e32 v81, 0xffff0000, v191
	v_pk_add_f32 v[74:75], v[74:75], v[86:87]
	v_pk_add_f32 v[78:79], v[78:79], v[84:85]
	v_pk_add_f32 v[76:77], v[76:77], v[82:83]
	v_pk_add_f32 v[72:73], v[72:73], v[80:81]
	s_waitcnt lgkmcnt(1)
	v_lshlrev_b32_e32 v86, 16, v192
	v_and_b32_e32 v87, 0xffff0000, v192
	v_lshlrev_b32_e32 v84, 16, v193
	v_and_b32_e32 v85, 0xffff0000, v193
	v_lshlrev_b32_e32 v82, 16, v194
	v_and_b32_e32 v83, 0xffff0000, v194
	v_lshlrev_b32_e32 v80, 16, v195
	v_and_b32_e32 v81, 0xffff0000, v195
	v_pk_add_f32 v[74:75], v[74:75], v[86:87]
	v_pk_add_f32 v[78:79], v[78:79], v[84:85]
	v_pk_add_f32 v[76:77], v[76:77], v[82:83]
	v_pk_add_f32 v[72:73], v[72:73], v[80:81]
	s_waitcnt lgkmcnt(0)
	v_lshlrev_b32_e32 v86, 16, v204
	v_and_b32_e32 v87, 0xffff0000, v204
	v_lshlrev_b32_e32 v84, 16, v205
	v_and_b32_e32 v85, 0xffff0000, v205
	v_lshlrev_b32_e32 v82, 16, v206
	v_and_b32_e32 v83, 0xffff0000, v206
	v_lshlrev_b32_e32 v80, 16, v207
	v_and_b32_e32 v81, 0xffff0000, v207
	v_pk_add_f32 v[74:75], v[74:75], v[86:87]
	v_pk_add_f32 v[78:79], v[78:79], v[84:85]
	v_pk_add_f32 v[76:77], v[76:77], v[82:83]
	v_pk_add_f32 v[72:73], v[72:73], v[80:81]
	s_cmp_eq_u32 s20, 0
	s_cbranch_scc0 .LBB0_826
	s_branch .Lmy_pool_done
.Lmy_pool_t2:
	ds_read_b128 v[112:115], v93
	ds_read_b128 v[188:191], v93 offset:272
	s_waitcnt lgkmcnt(1)
	v_lshlrev_b32_e32 v86, 16, v112
	v_and_b32_e32 v87, 0xffff0000, v112
	v_lshlrev_b32_e32 v84, 16, v113
	v_and_b32_e32 v85, 0xffff0000, v113
	v_lshlrev_b32_e32 v82, 16, v114
	v_and_b32_e32 v83, 0xffff0000, v114
	v_lshlrev_b32_e32 v80, 16, v115
	v_and_b32_e32 v81, 0xffff0000, v115
	v_pk_add_f32 v[74:75], v[74:75], v[86:87]
	v_pk_add_f32 v[78:79], v[78:79], v[84:85]
	v_pk_add_f32 v[76:77], v[76:77], v[82:83]
	v_pk_add_f32 v[72:73], v[72:73], v[80:81]
	s_waitcnt lgkmcnt(0)
	v_lshlrev_b32_e32 v86, 16, v188
	v_and_b32_e32 v87, 0xffff0000, v188
	v_lshlrev_b32_e32 v84, 16, v189
	v_and_b32_e32 v85, 0xffff0000, v189
	v_lshlrev_b32_e32 v82, 16, v190
	v_and_b32_e32 v83, 0xffff0000, v190
	v_lshlrev_b32_e32 v80, 16, v191
	v_and_b32_e32 v81, 0xffff0000, v191
	v_pk_add_f32 v[74:75], v[74:75], v[86:87]
	v_pk_add_f32 v[78:79], v[78:79], v[84:85]
	v_pk_add_f32 v[76:77], v[76:77], v[82:83]
	v_pk_add_f32 v[72:73], v[72:73], v[80:81]
.Lmy_pool_done:
	v_add_u32_e32 v92, s19, v92
	v_min_i32_e32 v92, s18, v92
	v_cvt_f32_i32_e32 v92, v92
	v_div_scale_f32 v93, s[20:21], v92, v92, 1.0
	v_rcp_f32_e32 v94, v93
	v_div_scale_f32 v95, vcc, 1.0, v92, 1.0
	s_movk_i32 s20, 0x5ff
	v_fma_f32 v112, -v93, v94, 1.0
	v_fmac_f32_e32 v94, v112, v94
	v_mul_f32_e32 v112, v95, v94
	v_fma_f32 v113, -v93, v112, v95
	v_fmac_f32_e32 v112, v113, v94
	v_fma_f32 v93, -v93, v112, v95
	v_div_fmas_f32 v93, v93, v94, v112
	v_div_fixup_f32 v92, v93, v92, 1.0
	v_fma_f32 v74, v92, v74, -v86
	v_fma_f32 v75, v92, v75, -v87
	v_cvt_pk_bf16_f32 v74, v74, v75
	v_fma_f32 v75, v92, v79, -v85
	v_fma_f32 v76, v92, v76, -v82
	v_fma_f32 v77, v92, v77, -v83
	v_fma_f32 v72, v92, v72, -v80
	v_fma_f32 v78, v92, v78, -v84
	v_cvt_pk_bf16_f32 v75, v78, v75
	v_cvt_pk_bf16_f32 v76, v76, v77
	v_fma_f32 v73, v92, v73, -v81
	v_cvt_pk_bf16_f32 v77, v72, v73
	v_add_u32_e32 v72, v41, v91
	ds_write_b128 v72, v[74:77] offset:39168
	v_add_u32_e32 v72, 0x200, v90
	v_cmp_lt_i32_e32 vcc, s20, v90
	s_or_b64 s[16:17], vcc, s[16:17]
	v_mov_b32_e32 v90, v72
	s_andn2_b64 exec, exec, s[16:17]
	s_cbranch_execnz .LBB0_825
	s_branch .LBB0_814

.LBB0_830:
	s_or_b64 exec, exec, s[4:5]
	v_lshlrev_b64 v[4:5], 2, v[28:29]
	v_readlane_b32 s4, v242, 46
	v_lshl_add_u64 v[8:9], v[22:23], 0, v[4:5]
	v_readlane_b32 s5, v242, 47
	v_or_b32_e32 v6, v6, v61
	v_readlane_b32 s16, v243, 24
	v_lshl_add_u64 v[10:11], v[8:9], 0, s[12:13]
	v_lshl_add_u64 v[12:13], v[8:9], 0, s[4:5]
	v_readlane_b32 s4, v242, 48
	v_ashrrev_i32_e32 v7, 31, v6
	v_readlane_b32 s24, v243, 32
	v_readlane_b32 s25, v243, 33
	s_waitcnt lgkmcnt(0)
	s_barrier
	v_lshl_add_u64 v[14:15], v[8:9], 0, s[0:1]
	v_lshl_add_u64 v[16:17], v[8:9], 0, s[82:83]
	v_lshl_add_u64 v[18:19], v[8:9], 0, s[8:9]
	v_lshl_add_u64 v[30:31], v[8:9], 0, s[90:91]
	v_lshl_add_u64 v[32:33], v[8:9], 0, s[50:51]
	v_lshl_add_u64 v[34:35], v[8:9], 0, s[2:3]
	global_load_dword v122, v[10:11], off
	global_load_dword v121, v[12:13], off
	global_load_dword v120, v[14:15], off
	global_load_dword v119, v[16:17], off
	global_load_dword v118, v[18:19], off
	global_load_dword v117, v[30:31], off
	global_load_dword v116, v[32:33], off
	global_load_dword v115, v[34:35], off
	v_lshl_add_u64 v[10:11], v[8:9], 0, s[14:15]
	v_readlane_b32 s5, v242, 49
	v_lshl_add_u64 v[6:7], v[6:7], 2, s[24:25]
	v_lshl_add_u64 v[14:15], v[8:9], 0, s[34:35]
	v_lshl_add_u64 v[12:13], v[8:9], 0, s[4:5]
	v_lshl_add_u64 v[16:17], v[8:9], 0, s[36:37]
	v_lshl_add_u64 v[18:19], v[8:9], 0, s[38:39]
	v_lshl_add_u64 v[30:31], v[8:9], 0, s[40:41]
	v_lshl_add_u64 v[32:33], v[8:9], 0, s[42:43]
	v_lshl_add_u64 v[34:35], v[8:9], 0, s[44:45]
	global_load_dword v131, v[10:11], off
	global_load_dword v130, v[12:13], off
	global_load_dword v129, v[14:15], off
	global_load_dword v128, v[16:17], off
	global_load_dword v126, v[18:19], off
	global_load_dword v125, v[30:31], off
	global_load_dword v124, v[32:33], off
	global_load_dword v123, v[34:35], off
	global_load_dword v127, v[6:7], off
	v_lshl_add_u64 v[6:7], v[8:9], 0, s[48:49]
	v_lshl_add_u64 v[10:11], v[8:9], 0, s[52:53]
	v_lshl_add_u64 v[12:13], v[8:9], 0, s[54:55]
	v_lshl_add_u64 v[14:15], v[8:9], 0, s[56:57]
	v_lshl_add_u64 v[16:17], v[8:9], 0, s[58:59]
	v_lshl_add_u64 v[18:19], v[8:9], 0, s[60:61]
	v_lshl_add_u64 v[30:31], v[8:9], 0, s[62:63]
	v_lshl_add_u64 v[32:33], v[8:9], 0, s[64:65]
	global_load_dword v146, v[6:7], off
	global_load_dword v144, v[10:11], off
	global_load_dword v142, v[12:13], off
	global_load_dword v140, v[14:15], off
	global_load_dword v138, v[16:17], off
	global_load_dword v136, v[18:19], off
	global_load_dword v134, v[30:31], off
	global_load_dword v132, v[32:33], off
	v_lshl_add_u64 v[6:7], v[8:9], 0, s[66:67]
	v_lshl_add_u64 v[10:11], v[8:9], 0, s[68:69]
	v_lshl_add_u64 v[12:13], v[8:9], 0, s[70:71]
	v_lshl_add_u64 v[14:15], v[8:9], 0, s[72:73]
	v_lshl_add_u64 v[16:17], v[8:9], 0, s[92:93]
	v_lshl_add_u64 v[18:19], v[8:9], 0, s[76:77]
	v_lshl_add_u64 v[8:9], v[8:9], 0, s[78:79]
	global_load_dword v145, v[6:7], off
	global_load_dword v143, v[10:11], off
	global_load_dword v141, v[12:13], off
	global_load_dword v139, v[14:15], off
	global_load_dword v137, v[16:17], off
	global_load_dword v135, v[18:19], off
	global_load_dword v133, v[8:9], off
	ds_read2st64_b32 v[148:149], v45 offset1:2
	ds_read2st64_b32 v[150:151], v45 offset0:4 offset1:6
	ds_read2st64_b32 v[94:95], v45 offset0:8 offset1:10
	ds_read2st64_b32 v[92:93], v45 offset0:12 offset1:14
	ds_read2st64_b32 v[90:91], v45 offset0:16 offset1:18
	ds_read2st64_b32 v[88:89], v45 offset0:20 offset1:22
	ds_read2st64_b32 v[86:87], v45 offset0:24 offset1:26
	ds_read2st64_b32 v[84:85], v45 offset0:28 offset1:30
	ds_read2st64_b32 v[82:83], v45 offset0:32 offset1:34
	ds_read2st64_b32 v[80:81], v45 offset0:36 offset1:38
	ds_read2st64_b32 v[78:79], v45 offset0:40 offset1:42
	ds_read2st64_b32 v[76:77], v45 offset0:44 offset1:46
	ds_read2st64_b32 v[74:75], v45 offset0:48 offset1:50
	ds_read2st64_b32 v[72:73], v45 offset0:52 offset1:54
	ds_read2st64_b32 v[70:71], v45 offset0:56 offset1:58
	ds_read2st64_b32 v[68:69], v45 offset0:60 offset1:62
	ds_read2st64_b32 v[66:67], v45 offset0:64 offset1:66
	ds_read2st64_b32 v[64:65], v45 offset0:68 offset1:70
	ds_read2st64_b32 v[58:59], v45 offset0:72 offset1:74
	ds_read2st64_b32 v[56:57], v45 offset0:76 offset1:78
	ds_read2st64_b32 v[42:43], v45 offset0:80 offset1:82
	ds_read2st64_b32 v[34:35], v45 offset0:84 offset1:86
	ds_read2st64_b32 v[32:33], v45 offset0:88 offset1:90
	ds_read2st64_b32 v[30:31], v45 offset0:92 offset1:94
	ds_read2st64_b32 v[18:19], v45 offset0:96 offset1:98
	ds_read2st64_b32 v[16:17], v45 offset0:100 offset1:102
	ds_read2st64_b32 v[14:15], v45 offset0:104 offset1:106
	ds_read2st64_b32 v[12:13], v45 offset0:108 offset1:110
	ds_read2st64_b32 v[10:11], v45 offset0:112 offset1:114
	ds_read2st64_b32 v[8:9], v45 offset0:116 offset1:118
	ds_read2st64_b32 v[6:7], v45 offset0:120 offset1:122
	s_waitcnt lgkmcnt(0)
	s_barrier
	s_mov_b32 s10, 0xf800000
	v_lshlrev_b64 v[28:29], 1, v[28:29]
	s_mov_b32 s11, 0x40e00000
	s_add_i32 s86, s86, s75
	s_cmpk_gt_i32 s86, 0xff
	v_readlane_b32 s17, v243, 25
	v_readlane_b32 s18, v243, 26
	v_readlane_b32 s19, v243, 27
	v_readlane_b32 s20, v243, 28
	v_readlane_b32 s21, v243, 29
	v_readlane_b32 s22, v243, 30
	v_readlane_b32 s23, v243, 31
	v_readlane_b32 s26, v243, 34
	v_readlane_b32 s27, v243, 35
	v_readlane_b32 s28, v243, 36
	v_readlane_b32 s29, v243, 37
	v_readlane_b32 s30, v243, 38
	v_readlane_b32 s31, v243, 39
	s_waitcnt vmcnt(15)
	v_fma_f32 v147, v122, v148, v127
	v_fmac_f32_e32 v147, v121, v149
	v_fma_f32 v148, v122, v149, v127
	v_fmac_f32_e32 v147, v120, v150
	v_fmac_f32_e32 v148, v121, v150
	v_fma_f32 v149, v122, v150, v127
	v_fmac_f32_e32 v147, v119, v151
	v_fmac_f32_e32 v148, v120, v151
	v_fmac_f32_e32 v149, v121, v151
	v_fma_f32 v150, v122, v151, v127
	v_fmac_f32_e32 v147, v118, v94
	v_fmac_f32_e32 v148, v119, v94
	v_fmac_f32_e32 v149, v120, v94
	v_fmac_f32_e32 v150, v121, v94
	v_fma_f32 v94, v122, v94, v127
	v_fmac_f32_e32 v147, v117, v95
	v_fmac_f32_e32 v148, v118, v95
	v_fmac_f32_e32 v149, v119, v95
	v_fmac_f32_e32 v150, v120, v95
	v_fmac_f32_e32 v94, v121, v95
	v_fma_f32 v95, v122, v95, v127
	v_fmac_f32_e32 v147, v116, v92
	v_fmac_f32_e32 v148, v117, v92
	v_fmac_f32_e32 v149, v118, v92
	v_fmac_f32_e32 v150, v119, v92
	v_fmac_f32_e32 v94, v120, v92
	v_fmac_f32_e32 v95, v121, v92
	v_fma_f32 v92, v122, v92, v127
	v_fmac_f32_e32 v147, v115, v93
	v_fmac_f32_e32 v148, v116, v93
	v_fmac_f32_e32 v149, v117, v93
	v_fmac_f32_e32 v150, v118, v93
	v_fmac_f32_e32 v94, v119, v93
	v_fmac_f32_e32 v95, v120, v93
	v_fmac_f32_e32 v92, v121, v93
	v_fma_f32 v93, v122, v93, v127
	v_fmac_f32_e32 v147, v131, v90
	v_fmac_f32_e32 v148, v115, v90
	v_fmac_f32_e32 v149, v116, v90
	v_fmac_f32_e32 v150, v117, v90
	v_fmac_f32_e32 v94, v118, v90
	v_fmac_f32_e32 v95, v119, v90
	v_fmac_f32_e32 v92, v120, v90
	v_fmac_f32_e32 v93, v121, v90
	v_fma_f32 v90, v122, v90, v127
	v_fmac_f32_e32 v147, v130, v91
	v_fmac_f32_e32 v148, v131, v91
	v_fmac_f32_e32 v149, v115, v91
	v_fmac_f32_e32 v150, v116, v91
	v_fmac_f32_e32 v94, v117, v91
	v_fmac_f32_e32 v95, v118, v91
	v_fmac_f32_e32 v92, v119, v91
	v_fmac_f32_e32 v93, v120, v91
	v_fmac_f32_e32 v90, v121, v91
	v_fma_f32 v91, v122, v91, v127
	v_fmac_f32_e32 v147, v129, v88
	v_fmac_f32_e32 v148, v130, v88
	v_fmac_f32_e32 v149, v131, v88
	v_fmac_f32_e32 v150, v115, v88
	v_fmac_f32_e32 v94, v116, v88
	v_fmac_f32_e32 v95, v117, v88
	v_fmac_f32_e32 v92, v118, v88
	v_fmac_f32_e32 v93, v119, v88
	v_fmac_f32_e32 v90, v120, v88
	v_fmac_f32_e32 v91, v121, v88
	v_fma_f32 v88, v122, v88, v127
	v_fmac_f32_e32 v147, v128, v89
	v_fmac_f32_e32 v148, v129, v89
	v_fmac_f32_e32 v149, v130, v89
	v_fmac_f32_e32 v150, v131, v89
	v_fmac_f32_e32 v94, v115, v89
	v_fmac_f32_e32 v95, v116, v89
	v_fmac_f32_e32 v92, v117, v89
	v_fmac_f32_e32 v93, v118, v89
	v_fmac_f32_e32 v90, v119, v89
	v_fmac_f32_e32 v91, v120, v89
	v_fmac_f32_e32 v88, v121, v89
	v_fma_f32 v89, v122, v89, v127
	v_fmac_f32_e32 v147, v126, v86
	v_fmac_f32_e32 v148, v128, v86
	v_fmac_f32_e32 v149, v129, v86
	v_fmac_f32_e32 v150, v130, v86
	v_fmac_f32_e32 v94, v131, v86
	v_fmac_f32_e32 v95, v115, v86
	v_fmac_f32_e32 v92, v116, v86
	v_fmac_f32_e32 v93, v117, v86
	v_fmac_f32_e32 v90, v118, v86
	v_fmac_f32_e32 v91, v119, v86
	v_fmac_f32_e32 v88, v120, v86
	v_fmac_f32_e32 v89, v121, v86
	v_fma_f32 v86, v122, v86, v127
	v_fmac_f32_e32 v147, v125, v87
	v_fmac_f32_e32 v148, v126, v87
	v_fmac_f32_e32 v149, v128, v87
	v_fmac_f32_e32 v150, v129, v87
	v_fmac_f32_e32 v94, v130, v87
	v_fmac_f32_e32 v95, v131, v87
	v_fmac_f32_e32 v92, v115, v87
	v_fmac_f32_e32 v93, v116, v87
	v_fmac_f32_e32 v90, v117, v87
	v_fmac_f32_e32 v91, v118, v87
	v_fmac_f32_e32 v88, v119, v87
	v_fmac_f32_e32 v89, v120, v87
	v_fmac_f32_e32 v86, v121, v87
	v_fma_f32 v87, v122, v87, v127
	v_fmac_f32_e32 v147, v124, v84
	v_fmac_f32_e32 v148, v125, v84
	v_fmac_f32_e32 v149, v126, v84
	v_fmac_f32_e32 v150, v128, v84
	v_fmac_f32_e32 v94, v129, v84
	v_fmac_f32_e32 v95, v130, v84
	v_fmac_f32_e32 v92, v131, v84
	v_fmac_f32_e32 v93, v115, v84
	v_fmac_f32_e32 v90, v116, v84
	v_fmac_f32_e32 v91, v117, v84
	v_fmac_f32_e32 v88, v118, v84
	v_fmac_f32_e32 v89, v119, v84
	v_fmac_f32_e32 v86, v120, v84
	v_fmac_f32_e32 v87, v121, v84
	v_fma_f32 v84, v122, v84, v127
	v_fmac_f32_e32 v147, v123, v85
	v_fmac_f32_e32 v148, v124, v85
	v_fmac_f32_e32 v149, v125, v85
	v_fmac_f32_e32 v150, v126, v85
	v_fmac_f32_e32 v94, v128, v85
	v_fmac_f32_e32 v95, v129, v85
	v_fmac_f32_e32 v92, v130, v85
	v_fmac_f32_e32 v93, v131, v85
	v_fmac_f32_e32 v90, v115, v85
	v_fmac_f32_e32 v91, v116, v85
	v_fmac_f32_e32 v88, v117, v85
	v_fmac_f32_e32 v89, v118, v85
	v_fmac_f32_e32 v86, v119, v85
	v_fmac_f32_e32 v87, v120, v85
	v_fmac_f32_e32 v84, v121, v85
	v_fma_f32 v85, v122, v85, v127
	s_waitcnt vmcnt(14)
	v_fmac_f32_e32 v147, v146, v82
	v_fmac_f32_e32 v148, v123, v82
	v_fmac_f32_e32 v149, v124, v82
	v_fmac_f32_e32 v150, v125, v82
	v_fmac_f32_e32 v94, v126, v82
	v_fmac_f32_e32 v95, v128, v82
	v_fmac_f32_e32 v92, v129, v82
	v_fmac_f32_e32 v93, v130, v82
	v_fmac_f32_e32 v90, v131, v82
	v_fmac_f32_e32 v91, v115, v82
	v_fmac_f32_e32 v88, v116, v82
	v_fmac_f32_e32 v89, v117, v82
	v_fmac_f32_e32 v86, v118, v82
	v_fmac_f32_e32 v87, v119, v82
	v_fmac_f32_e32 v84, v120, v82
	v_fmac_f32_e32 v85, v121, v82
	v_fma_f32 v82, v122, v82, v127
	s_waitcnt vmcnt(13)
	v_fmac_f32_e32 v147, v144, v83
	v_fmac_f32_e32 v148, v146, v83
	v_fmac_f32_e32 v149, v123, v83
	v_fmac_f32_e32 v150, v124, v83
	v_fmac_f32_e32 v94, v125, v83
	v_fmac_f32_e32 v95, v126, v83
	v_fmac_f32_e32 v92, v128, v83
	v_fmac_f32_e32 v93, v129, v83
	v_fmac_f32_e32 v90, v130, v83
	v_fmac_f32_e32 v91, v131, v83
	v_fmac_f32_e32 v88, v115, v83
	v_fmac_f32_e32 v89, v116, v83
	v_fmac_f32_e32 v86, v117, v83
	v_fmac_f32_e32 v87, v118, v83
	v_fmac_f32_e32 v84, v119, v83
	v_fmac_f32_e32 v85, v120, v83
	v_fmac_f32_e32 v82, v121, v83
	v_fma_f32 v83, v122, v83, v127
	s_waitcnt vmcnt(12)
	v_fmac_f32_e32 v147, v142, v80
	v_fmac_f32_e32 v148, v144, v80
	v_fmac_f32_e32 v149, v146, v80
	v_fmac_f32_e32 v150, v123, v80
	v_fmac_f32_e32 v94, v124, v80
	v_fmac_f32_e32 v95, v125, v80
	v_fmac_f32_e32 v92, v126, v80
	v_fmac_f32_e32 v93, v128, v80
	v_fmac_f32_e32 v90, v129, v80
	v_fmac_f32_e32 v91, v130, v80
	v_fmac_f32_e32 v88, v131, v80
	v_fmac_f32_e32 v89, v115, v80
	v_fmac_f32_e32 v86, v116, v80
	v_fmac_f32_e32 v87, v117, v80
	v_fmac_f32_e32 v84, v118, v80
	v_fmac_f32_e32 v85, v119, v80
	v_fmac_f32_e32 v82, v120, v80
	v_fmac_f32_e32 v83, v121, v80
	v_fma_f32 v80, v122, v80, v127
	s_waitcnt vmcnt(11)
	v_fmac_f32_e32 v147, v140, v81
	v_fmac_f32_e32 v148, v142, v81
	v_fmac_f32_e32 v149, v144, v81
	v_fmac_f32_e32 v150, v146, v81
	v_fmac_f32_e32 v94, v123, v81
	v_fmac_f32_e32 v95, v124, v81
	v_fmac_f32_e32 v92, v125, v81
	v_fmac_f32_e32 v93, v126, v81
	v_fmac_f32_e32 v90, v128, v81
	v_fmac_f32_e32 v91, v129, v81
	v_fmac_f32_e32 v88, v130, v81
	v_fmac_f32_e32 v89, v131, v81
	v_fmac_f32_e32 v86, v115, v81
	v_fmac_f32_e32 v87, v116, v81
	v_fmac_f32_e32 v84, v117, v81
	v_fmac_f32_e32 v85, v118, v81
	v_fmac_f32_e32 v82, v119, v81
	v_fmac_f32_e32 v83, v120, v81
	v_fmac_f32_e32 v80, v121, v81
	v_fma_f32 v81, v122, v81, v127
	s_waitcnt vmcnt(10)
	v_fmac_f32_e32 v147, v138, v78
	v_fmac_f32_e32 v148, v140, v78
	v_fmac_f32_e32 v149, v142, v78
	v_fmac_f32_e32 v150, v144, v78
	v_fmac_f32_e32 v94, v146, v78
	v_fmac_f32_e32 v95, v123, v78
	v_fmac_f32_e32 v92, v124, v78
	v_fmac_f32_e32 v93, v125, v78
	v_fmac_f32_e32 v90, v126, v78
	v_fmac_f32_e32 v91, v128, v78
	v_fmac_f32_e32 v88, v129, v78
	v_fmac_f32_e32 v89, v130, v78
	v_fmac_f32_e32 v86, v131, v78
	v_fmac_f32_e32 v87, v115, v78
	v_fmac_f32_e32 v84, v116, v78
	v_fmac_f32_e32 v85, v117, v78
	v_fmac_f32_e32 v82, v118, v78
	v_fmac_f32_e32 v83, v119, v78
	v_fmac_f32_e32 v80, v120, v78
	v_fmac_f32_e32 v81, v121, v78
	v_fma_f32 v78, v122, v78, v127
	s_waitcnt vmcnt(9)
	v_fmac_f32_e32 v147, v136, v79
	v_fmac_f32_e32 v148, v138, v79
	v_fmac_f32_e32 v149, v140, v79
	v_fmac_f32_e32 v150, v142, v79
	v_fmac_f32_e32 v94, v144, v79
	v_fmac_f32_e32 v95, v146, v79
	v_fmac_f32_e32 v92, v123, v79
	v_fmac_f32_e32 v93, v124, v79
	v_fmac_f32_e32 v90, v125, v79
	v_fmac_f32_e32 v91, v126, v79
	v_fmac_f32_e32 v88, v128, v79
	v_fmac_f32_e32 v89, v129, v79
	v_fmac_f32_e32 v86, v130, v79
	v_fmac_f32_e32 v87, v131, v79
	v_fmac_f32_e32 v84, v115, v79
	v_fmac_f32_e32 v85, v116, v79
	v_fmac_f32_e32 v82, v117, v79
	v_fmac_f32_e32 v83, v118, v79
	v_fmac_f32_e32 v80, v119, v79
	v_fmac_f32_e32 v81, v120, v79
	v_fmac_f32_e32 v78, v121, v79
	v_fma_f32 v79, v122, v79, v127
	s_waitcnt vmcnt(8)
	v_fmac_f32_e32 v147, v134, v76
	v_fmac_f32_e32 v148, v136, v76
	v_fmac_f32_e32 v149, v138, v76
	v_fmac_f32_e32 v150, v140, v76
	v_fmac_f32_e32 v94, v142, v76
	v_fmac_f32_e32 v95, v144, v76
	v_fmac_f32_e32 v92, v146, v76
	v_fmac_f32_e32 v93, v123, v76
	v_fmac_f32_e32 v90, v124, v76
	v_fmac_f32_e32 v91, v125, v76
	v_fmac_f32_e32 v88, v126, v76
	v_fmac_f32_e32 v89, v128, v76
	v_fmac_f32_e32 v86, v129, v76
	v_fmac_f32_e32 v87, v130, v76
	v_fmac_f32_e32 v84, v131, v76
	v_fmac_f32_e32 v85, v115, v76
	v_fmac_f32_e32 v82, v116, v76
	v_fmac_f32_e32 v83, v117, v76
	v_fmac_f32_e32 v80, v118, v76
	v_fmac_f32_e32 v81, v119, v76
	v_fmac_f32_e32 v78, v120, v76
	v_fmac_f32_e32 v79, v121, v76
	v_fma_f32 v76, v122, v76, v127
	s_waitcnt vmcnt(7)
	v_fmac_f32_e32 v147, v132, v77
	v_fmac_f32_e32 v148, v134, v77
	v_fmac_f32_e32 v149, v136, v77
	v_fmac_f32_e32 v150, v138, v77
	v_fmac_f32_e32 v94, v140, v77
	v_fmac_f32_e32 v95, v142, v77
	v_fmac_f32_e32 v92, v144, v77
	v_fmac_f32_e32 v93, v146, v77
	v_fmac_f32_e32 v90, v123, v77
	v_fmac_f32_e32 v91, v124, v77
	v_fmac_f32_e32 v88, v125, v77
	v_fmac_f32_e32 v89, v126, v77
	v_fmac_f32_e32 v86, v128, v77
	v_fmac_f32_e32 v87, v129, v77
	v_fmac_f32_e32 v84, v130, v77
	v_fmac_f32_e32 v85, v131, v77
	v_fmac_f32_e32 v82, v115, v77
	v_fmac_f32_e32 v83, v116, v77
	v_fmac_f32_e32 v80, v117, v77
	v_fmac_f32_e32 v81, v118, v77
	v_fmac_f32_e32 v78, v119, v77
	v_fmac_f32_e32 v79, v120, v77
	v_fmac_f32_e32 v76, v121, v77
	v_fma_f32 v77, v122, v77, v127
	s_waitcnt vmcnt(6)
	v_fmac_f32_e32 v147, v145, v74
	v_fmac_f32_e32 v148, v132, v74
	v_fmac_f32_e32 v149, v134, v74
	v_fmac_f32_e32 v150, v136, v74
	v_fmac_f32_e32 v94, v138, v74
	v_fmac_f32_e32 v95, v140, v74
	v_fmac_f32_e32 v92, v142, v74
	v_fmac_f32_e32 v93, v144, v74
	v_fmac_f32_e32 v90, v146, v74
	v_fmac_f32_e32 v91, v123, v74
	v_fmac_f32_e32 v88, v124, v74
	v_fmac_f32_e32 v89, v125, v74
	v_fmac_f32_e32 v86, v126, v74
	v_fmac_f32_e32 v87, v128, v74
	v_fmac_f32_e32 v84, v129, v74
	v_fmac_f32_e32 v85, v130, v74
	v_fmac_f32_e32 v82, v131, v74
	v_fmac_f32_e32 v83, v115, v74
	v_fmac_f32_e32 v80, v116, v74
	v_fmac_f32_e32 v81, v117, v74
	v_fmac_f32_e32 v78, v118, v74
	v_fmac_f32_e32 v79, v119, v74
	v_fmac_f32_e32 v76, v120, v74
	v_fmac_f32_e32 v77, v121, v74
	v_fma_f32 v74, v122, v74, v127
	s_waitcnt vmcnt(5)
	v_fmac_f32_e32 v147, v143, v75
	v_fmac_f32_e32 v148, v145, v75
	v_fmac_f32_e32 v149, v132, v75
	v_fmac_f32_e32 v150, v134, v75
	v_fmac_f32_e32 v94, v136, v75
	v_fmac_f32_e32 v95, v138, v75
	v_fmac_f32_e32 v92, v140, v75
	v_fmac_f32_e32 v93, v142, v75
	v_fmac_f32_e32 v90, v144, v75
	v_fmac_f32_e32 v91, v146, v75
	v_fmac_f32_e32 v88, v123, v75
	v_fmac_f32_e32 v89, v124, v75
	v_fmac_f32_e32 v86, v125, v75
	v_fmac_f32_e32 v87, v126, v75
	v_fmac_f32_e32 v84, v128, v75
	v_fmac_f32_e32 v85, v129, v75
	v_fmac_f32_e32 v82, v130, v75
	v_fmac_f32_e32 v83, v131, v75
	v_fmac_f32_e32 v80, v115, v75
	v_fmac_f32_e32 v81, v116, v75
	v_fmac_f32_e32 v78, v117, v75
	v_fmac_f32_e32 v79, v118, v75
	v_fmac_f32_e32 v76, v119, v75
	v_fmac_f32_e32 v77, v120, v75
	v_fmac_f32_e32 v74, v121, v75
	v_fma_f32 v75, v122, v75, v127
	s_waitcnt vmcnt(4)
	v_fmac_f32_e32 v147, v141, v72
	v_fmac_f32_e32 v148, v143, v72
	v_fmac_f32_e32 v149, v145, v72
	v_fmac_f32_e32 v150, v132, v72
	v_fmac_f32_e32 v94, v134, v72
	v_fmac_f32_e32 v95, v136, v72
	v_fmac_f32_e32 v92, v138, v72
	v_fmac_f32_e32 v93, v140, v72
	v_fmac_f32_e32 v90, v142, v72
	v_fmac_f32_e32 v91, v144, v72
	v_fmac_f32_e32 v88, v146, v72
	v_fmac_f32_e32 v89, v123, v72
	v_fmac_f32_e32 v86, v124, v72
	v_fmac_f32_e32 v87, v125, v72
	v_fmac_f32_e32 v84, v126, v72
	v_fmac_f32_e32 v85, v128, v72
	v_fmac_f32_e32 v82, v129, v72
	v_fmac_f32_e32 v83, v130, v72
	v_fmac_f32_e32 v80, v131, v72
	v_fmac_f32_e32 v81, v115, v72
	v_fmac_f32_e32 v78, v116, v72
	v_fmac_f32_e32 v79, v117, v72
	v_fmac_f32_e32 v76, v118, v72
	v_fmac_f32_e32 v77, v119, v72
	v_fmac_f32_e32 v74, v120, v72
	v_fmac_f32_e32 v75, v121, v72
	v_fma_f32 v72, v122, v72, v127
	s_waitcnt vmcnt(3)
	v_fmac_f32_e32 v147, v139, v73
	v_fmac_f32_e32 v148, v141, v73
	v_fmac_f32_e32 v149, v143, v73
	v_fmac_f32_e32 v150, v145, v73
	v_fmac_f32_e32 v94, v132, v73
	v_fmac_f32_e32 v95, v134, v73
	v_fmac_f32_e32 v92, v136, v73
	v_fmac_f32_e32 v93, v138, v73
	v_fmac_f32_e32 v90, v140, v73
	v_fmac_f32_e32 v91, v142, v73
	v_fmac_f32_e32 v88, v144, v73
	v_fmac_f32_e32 v89, v146, v73
	v_fmac_f32_e32 v86, v123, v73
	v_fmac_f32_e32 v87, v124, v73
	v_fmac_f32_e32 v84, v125, v73
	v_fmac_f32_e32 v85, v126, v73
	v_fmac_f32_e32 v82, v128, v73
	v_fmac_f32_e32 v83, v129, v73
	v_fmac_f32_e32 v80, v130, v73
	v_fmac_f32_e32 v81, v131, v73
	v_fmac_f32_e32 v78, v115, v73
	v_fmac_f32_e32 v79, v116, v73
	v_fmac_f32_e32 v76, v117, v73
	v_fmac_f32_e32 v77, v118, v73
	v_fmac_f32_e32 v74, v119, v73
	v_fmac_f32_e32 v75, v120, v73
	v_fmac_f32_e32 v72, v121, v73
	v_fma_f32 v73, v122, v73, v127
	s_waitcnt vmcnt(2)
	v_fmac_f32_e32 v147, v137, v70
	v_fmac_f32_e32 v148, v139, v70
	v_fmac_f32_e32 v149, v141, v70
	v_fmac_f32_e32 v150, v143, v70
	v_fmac_f32_e32 v94, v145, v70
	v_fmac_f32_e32 v95, v132, v70
	v_fmac_f32_e32 v92, v134, v70
	v_fmac_f32_e32 v93, v136, v70
	v_fmac_f32_e32 v90, v138, v70
	v_fmac_f32_e32 v91, v140, v70
	v_fmac_f32_e32 v88, v142, v70
	v_fmac_f32_e32 v89, v144, v70
	v_fmac_f32_e32 v86, v146, v70
	v_fmac_f32_e32 v87, v123, v70
	v_fmac_f32_e32 v84, v124, v70
	v_fmac_f32_e32 v85, v125, v70
	v_fmac_f32_e32 v82, v126, v70
	v_fmac_f32_e32 v83, v128, v70
	v_fmac_f32_e32 v80, v129, v70
	v_fmac_f32_e32 v81, v130, v70
	v_fmac_f32_e32 v78, v131, v70
	v_fmac_f32_e32 v79, v115, v70
	v_fmac_f32_e32 v76, v116, v70
	v_fmac_f32_e32 v77, v117, v70
	v_fmac_f32_e32 v74, v118, v70
	v_fmac_f32_e32 v75, v119, v70
	v_fmac_f32_e32 v72, v120, v70
	v_fmac_f32_e32 v73, v121, v70
	v_fma_f32 v70, v122, v70, v127
	s_waitcnt vmcnt(1)
	v_fmac_f32_e32 v147, v135, v71
	v_fmac_f32_e32 v148, v137, v71
	v_fmac_f32_e32 v149, v139, v71
	v_fmac_f32_e32 v150, v141, v71
	v_fmac_f32_e32 v94, v143, v71
	v_fmac_f32_e32 v95, v145, v71
	v_fmac_f32_e32 v92, v132, v71
	v_fmac_f32_e32 v93, v134, v71
	v_fmac_f32_e32 v90, v136, v71
	v_fmac_f32_e32 v91, v138, v71
	v_fmac_f32_e32 v88, v140, v71
	v_fmac_f32_e32 v89, v142, v71
	v_fmac_f32_e32 v86, v144, v71
	v_fmac_f32_e32 v87, v146, v71
	v_fmac_f32_e32 v84, v123, v71
	v_fmac_f32_e32 v85, v124, v71
	v_fmac_f32_e32 v82, v125, v71
	v_fmac_f32_e32 v83, v126, v71
	v_fmac_f32_e32 v80, v128, v71
	v_fmac_f32_e32 v81, v129, v71
	v_fmac_f32_e32 v78, v130, v71
	v_fmac_f32_e32 v79, v131, v71
	v_fmac_f32_e32 v76, v115, v71
	v_fmac_f32_e32 v77, v116, v71
	v_fmac_f32_e32 v74, v117, v71
	v_fmac_f32_e32 v75, v118, v71
	v_fmac_f32_e32 v72, v119, v71
	v_fmac_f32_e32 v73, v120, v71
	v_fmac_f32_e32 v70, v121, v71
	v_fma_f32 v71, v122, v71, v127
	s_waitcnt vmcnt(0)
	v_fmac_f32_e32 v147, v133, v68
	v_fmac_f32_e32 v148, v135, v68
	v_fmac_f32_e32 v149, v137, v68
	v_fmac_f32_e32 v150, v139, v68
	v_fmac_f32_e32 v94, v141, v68
	v_fmac_f32_e32 v95, v143, v68
	v_fmac_f32_e32 v92, v145, v68
	v_fmac_f32_e32 v93, v132, v68
	v_fmac_f32_e32 v90, v134, v68
	v_fmac_f32_e32 v91, v136, v68
	v_fmac_f32_e32 v88, v138, v68
	v_fmac_f32_e32 v89, v140, v68
	v_fmac_f32_e32 v86, v142, v68
	v_fmac_f32_e32 v87, v144, v68
	v_fmac_f32_e32 v84, v146, v68
	v_fmac_f32_e32 v85, v123, v68
	v_fmac_f32_e32 v82, v124, v68
	v_fmac_f32_e32 v83, v125, v68
	v_fmac_f32_e32 v80, v126, v68
	v_fmac_f32_e32 v81, v128, v68
	v_fmac_f32_e32 v78, v129, v68
	v_fmac_f32_e32 v79, v130, v68
	v_fmac_f32_e32 v76, v131, v68
	v_fmac_f32_e32 v77, v115, v68
	v_fmac_f32_e32 v74, v116, v68
	v_fmac_f32_e32 v75, v117, v68
	v_fmac_f32_e32 v72, v118, v68
	v_fmac_f32_e32 v73, v119, v68
	v_fmac_f32_e32 v70, v120, v68
	v_fmac_f32_e32 v71, v121, v68
	v_fma_f32 v68, v122, v68, v127
	v_fmac_f32_e32 v127, v122, v69
	v_fmac_f32_e32 v68, v121, v69
	v_fmac_f32_e32 v127, v121, v66
	v_fmac_f32_e32 v71, v120, v69
	v_fmac_f32_e32 v68, v120, v66
	v_fmac_f32_e32 v127, v120, v67
	v_fmac_f32_e32 v70, v119, v69
	v_fmac_f32_e32 v71, v119, v66
	v_fmac_f32_e32 v68, v119, v67
	v_fmac_f32_e32 v127, v119, v64
	v_fmac_f32_e32 v73, v118, v69
	v_fmac_f32_e32 v70, v118, v66
	v_fmac_f32_e32 v71, v118, v67
	v_fmac_f32_e32 v68, v118, v64
	v_fmac_f32_e32 v127, v118, v65
	v_fmac_f32_e32 v72, v117, v69
	v_fmac_f32_e32 v73, v117, v66
	v_fmac_f32_e32 v70, v117, v67
	v_fmac_f32_e32 v71, v117, v64
	v_fmac_f32_e32 v68, v117, v65
	v_fmac_f32_e32 v127, v117, v58
	v_fmac_f32_e32 v75, v116, v69
	v_fmac_f32_e32 v72, v116, v66
	v_fmac_f32_e32 v73, v116, v67
	v_fmac_f32_e32 v70, v116, v64
	v_fmac_f32_e32 v71, v116, v65
	v_fmac_f32_e32 v68, v116, v58
	v_fmac_f32_e32 v127, v116, v59
	v_fmac_f32_e32 v74, v115, v69
	v_fmac_f32_e32 v75, v115, v66
	v_fmac_f32_e32 v72, v115, v67
	v_fmac_f32_e32 v73, v115, v64
	v_fmac_f32_e32 v70, v115, v65
	v_fmac_f32_e32 v71, v115, v58
	v_fmac_f32_e32 v68, v115, v59
	v_fmac_f32_e32 v127, v115, v56
	v_fmac_f32_e32 v77, v131, v69
	v_fmac_f32_e32 v74, v131, v66
	v_fmac_f32_e32 v75, v131, v67
	v_fmac_f32_e32 v72, v131, v64
	v_fmac_f32_e32 v73, v131, v65
	v_fmac_f32_e32 v70, v131, v58
	v_fmac_f32_e32 v71, v131, v59
	v_fmac_f32_e32 v68, v131, v56
	v_fmac_f32_e32 v127, v131, v57
	v_fmac_f32_e32 v76, v130, v69
	v_fmac_f32_e32 v77, v130, v66
	v_fmac_f32_e32 v74, v130, v67
	v_fmac_f32_e32 v75, v130, v64
	v_fmac_f32_e32 v72, v130, v65
	v_fmac_f32_e32 v73, v130, v58
	v_fmac_f32_e32 v70, v130, v59
	v_fmac_f32_e32 v71, v130, v56
	v_fmac_f32_e32 v68, v130, v57
	v_fmac_f32_e32 v127, v130, v42
	v_fmac_f32_e32 v79, v129, v69
	v_fmac_f32_e32 v76, v129, v66
	v_fmac_f32_e32 v77, v129, v67
	v_fmac_f32_e32 v74, v129, v64
	v_fmac_f32_e32 v75, v129, v65
	v_fmac_f32_e32 v72, v129, v58
	v_fmac_f32_e32 v73, v129, v59
	v_fmac_f32_e32 v70, v129, v56
	v_fmac_f32_e32 v71, v129, v57
	v_fmac_f32_e32 v68, v129, v42
	v_fmac_f32_e32 v127, v129, v43
	v_fmac_f32_e32 v78, v128, v69
	v_fmac_f32_e32 v79, v128, v66
	v_fmac_f32_e32 v76, v128, v67
	v_fmac_f32_e32 v77, v128, v64
	v_fmac_f32_e32 v74, v128, v65
	v_fmac_f32_e32 v75, v128, v58
	v_fmac_f32_e32 v72, v128, v59
	v_fmac_f32_e32 v73, v128, v56
	v_fmac_f32_e32 v70, v128, v57
	v_fmac_f32_e32 v71, v128, v42
	v_fmac_f32_e32 v68, v128, v43
	v_fmac_f32_e32 v127, v128, v34
	v_fmac_f32_e32 v81, v126, v69
	v_fmac_f32_e32 v78, v126, v66
	v_fmac_f32_e32 v79, v126, v67
	v_fmac_f32_e32 v76, v126, v64
	v_fmac_f32_e32 v77, v126, v65
	v_fmac_f32_e32 v74, v126, v58
	v_fmac_f32_e32 v75, v126, v59
	v_fmac_f32_e32 v72, v126, v56
	v_fmac_f32_e32 v73, v126, v57
	v_fmac_f32_e32 v70, v126, v42
	v_fmac_f32_e32 v71, v126, v43
	v_fmac_f32_e32 v68, v126, v34
	v_fmac_f32_e32 v127, v126, v35
	v_fmac_f32_e32 v80, v125, v69
	v_fmac_f32_e32 v81, v125, v66
	v_fmac_f32_e32 v78, v125, v67
	v_fmac_f32_e32 v79, v125, v64
	v_fmac_f32_e32 v76, v125, v65
	v_fmac_f32_e32 v77, v125, v58
	v_fmac_f32_e32 v74, v125, v59
	v_fmac_f32_e32 v75, v125, v56
	v_fmac_f32_e32 v72, v125, v57
	v_fmac_f32_e32 v73, v125, v42
	v_fmac_f32_e32 v70, v125, v43
	v_fmac_f32_e32 v71, v125, v34
	v_fmac_f32_e32 v68, v125, v35
	v_fmac_f32_e32 v127, v125, v32
	v_fmac_f32_e32 v83, v124, v69
	v_fmac_f32_e32 v80, v124, v66
	v_fmac_f32_e32 v81, v124, v67
	v_fmac_f32_e32 v78, v124, v64
	v_fmac_f32_e32 v79, v124, v65
	v_fmac_f32_e32 v76, v124, v58
	v_fmac_f32_e32 v77, v124, v59
	v_fmac_f32_e32 v74, v124, v56
	v_fmac_f32_e32 v75, v124, v57
	v_fmac_f32_e32 v72, v124, v42
	v_fmac_f32_e32 v73, v124, v43
	v_fmac_f32_e32 v70, v124, v34
	v_fmac_f32_e32 v71, v124, v35
	v_fmac_f32_e32 v68, v124, v32
	v_fmac_f32_e32 v127, v124, v33
	v_fmac_f32_e32 v82, v123, v69
	v_fmac_f32_e32 v83, v123, v66
	v_fmac_f32_e32 v80, v123, v67
	v_fmac_f32_e32 v81, v123, v64
	v_fmac_f32_e32 v78, v123, v65
	v_fmac_f32_e32 v79, v123, v58
	v_fmac_f32_e32 v76, v123, v59
	v_fmac_f32_e32 v77, v123, v56
	v_fmac_f32_e32 v74, v123, v57
	v_fmac_f32_e32 v75, v123, v42
	v_fmac_f32_e32 v72, v123, v43
	v_fmac_f32_e32 v73, v123, v34
	v_fmac_f32_e32 v70, v123, v35
	v_fmac_f32_e32 v71, v123, v32
	v_fmac_f32_e32 v68, v123, v33
	v_fmac_f32_e32 v127, v123, v30
	v_fmac_f32_e32 v85, v146, v69
	v_fmac_f32_e32 v82, v146, v66
	v_fmac_f32_e32 v83, v146, v67
	v_fmac_f32_e32 v80, v146, v64
	v_fmac_f32_e32 v81, v146, v65
	v_fmac_f32_e32 v78, v146, v58
	v_fmac_f32_e32 v79, v146, v59
	v_fmac_f32_e32 v76, v146, v56
	v_fmac_f32_e32 v77, v146, v57
	v_fmac_f32_e32 v74, v146, v42
	v_fmac_f32_e32 v75, v146, v43
	v_fmac_f32_e32 v72, v146, v34
	v_fmac_f32_e32 v73, v146, v35
	v_fmac_f32_e32 v70, v146, v32
	v_fmac_f32_e32 v71, v146, v33
	v_fmac_f32_e32 v68, v146, v30
	v_fmac_f32_e32 v127, v146, v31
	v_fmac_f32_e32 v84, v144, v69
	v_fmac_f32_e32 v85, v144, v66
	v_fmac_f32_e32 v82, v144, v67
	v_fmac_f32_e32 v83, v144, v64
	v_fmac_f32_e32 v80, v144, v65
	v_fmac_f32_e32 v81, v144, v58
	v_fmac_f32_e32 v78, v144, v59
	v_fmac_f32_e32 v79, v144, v56
	v_fmac_f32_e32 v76, v144, v57
	v_fmac_f32_e32 v77, v144, v42
	v_fmac_f32_e32 v74, v144, v43
	v_fmac_f32_e32 v75, v144, v34
	v_fmac_f32_e32 v72, v144, v35
	v_fmac_f32_e32 v73, v144, v32
	v_fmac_f32_e32 v70, v144, v33
	v_fmac_f32_e32 v71, v144, v30
	v_fmac_f32_e32 v68, v144, v31
	v_fmac_f32_e32 v127, v144, v18
	v_fmac_f32_e32 v87, v142, v69
	v_fmac_f32_e32 v84, v142, v66
	v_fmac_f32_e32 v85, v142, v67
	v_fmac_f32_e32 v82, v142, v64
	v_fmac_f32_e32 v83, v142, v65
	v_fmac_f32_e32 v80, v142, v58
	v_fmac_f32_e32 v81, v142, v59
	v_fmac_f32_e32 v78, v142, v56
	v_fmac_f32_e32 v79, v142, v57
	v_fmac_f32_e32 v76, v142, v42
	v_fmac_f32_e32 v77, v142, v43
	v_fmac_f32_e32 v74, v142, v34
	v_fmac_f32_e32 v75, v142, v35
	v_fmac_f32_e32 v72, v142, v32
	v_fmac_f32_e32 v73, v142, v33
	v_fmac_f32_e32 v70, v142, v30
	v_fmac_f32_e32 v71, v142, v31
	v_fmac_f32_e32 v68, v142, v18
	v_fmac_f32_e32 v127, v142, v19
	v_fmac_f32_e32 v86, v140, v69
	v_fmac_f32_e32 v87, v140, v66
	v_fmac_f32_e32 v84, v140, v67
	v_fmac_f32_e32 v85, v140, v64
	v_fmac_f32_e32 v82, v140, v65
	v_fmac_f32_e32 v83, v140, v58
	v_fmac_f32_e32 v80, v140, v59
	v_fmac_f32_e32 v81, v140, v56
	v_fmac_f32_e32 v78, v140, v57
	v_fmac_f32_e32 v79, v140, v42
	v_fmac_f32_e32 v76, v140, v43
	v_fmac_f32_e32 v77, v140, v34
	v_fmac_f32_e32 v74, v140, v35
	v_fmac_f32_e32 v75, v140, v32
	v_fmac_f32_e32 v72, v140, v33
	v_fmac_f32_e32 v73, v140, v30
	v_fmac_f32_e32 v70, v140, v31
	v_fmac_f32_e32 v71, v140, v18
	v_fmac_f32_e32 v68, v140, v19
	v_fmac_f32_e32 v127, v140, v16
	v_fmac_f32_e32 v89, v138, v69
	v_fmac_f32_e32 v86, v138, v66
	v_fmac_f32_e32 v87, v138, v67
	v_fmac_f32_e32 v84, v138, v64
	v_fmac_f32_e32 v85, v138, v65
	v_fmac_f32_e32 v82, v138, v58
	v_fmac_f32_e32 v83, v138, v59
	v_fmac_f32_e32 v80, v138, v56
	v_fmac_f32_e32 v81, v138, v57
	v_fmac_f32_e32 v78, v138, v42
	v_fmac_f32_e32 v79, v138, v43
	v_fmac_f32_e32 v76, v138, v34
	v_fmac_f32_e32 v77, v138, v35
	v_fmac_f32_e32 v74, v138, v32
	v_fmac_f32_e32 v75, v138, v33
	v_fmac_f32_e32 v72, v138, v30
	v_fmac_f32_e32 v73, v138, v31
	v_fmac_f32_e32 v70, v138, v18
	v_fmac_f32_e32 v71, v138, v19
	v_fmac_f32_e32 v68, v138, v16
	v_fmac_f32_e32 v127, v138, v17
	v_fmac_f32_e32 v88, v136, v69
	v_fmac_f32_e32 v89, v136, v66
	v_fmac_f32_e32 v86, v136, v67
	v_fmac_f32_e32 v87, v136, v64
	v_fmac_f32_e32 v84, v136, v65
	v_fmac_f32_e32 v85, v136, v58
	v_fmac_f32_e32 v82, v136, v59
	v_fmac_f32_e32 v83, v136, v56
	v_fmac_f32_e32 v80, v136, v57
	v_fmac_f32_e32 v81, v136, v42
	v_fmac_f32_e32 v78, v136, v43
	v_fmac_f32_e32 v79, v136, v34
	v_fmac_f32_e32 v76, v136, v35
	v_fmac_f32_e32 v77, v136, v32
	v_fmac_f32_e32 v74, v136, v33
	v_fmac_f32_e32 v75, v136, v30
	v_fmac_f32_e32 v72, v136, v31
	v_fmac_f32_e32 v73, v136, v18
	v_fmac_f32_e32 v70, v136, v19
	v_fmac_f32_e32 v71, v136, v16
	v_fmac_f32_e32 v68, v136, v17
	v_fmac_f32_e32 v127, v136, v14
	v_fmac_f32_e32 v91, v134, v69
	v_fmac_f32_e32 v88, v134, v66
	v_fmac_f32_e32 v89, v134, v67
	v_fmac_f32_e32 v86, v134, v64
	v_fmac_f32_e32 v87, v134, v65
	v_fmac_f32_e32 v84, v134, v58
	v_fmac_f32_e32 v85, v134, v59
	v_fmac_f32_e32 v82, v134, v56
	v_fmac_f32_e32 v83, v134, v57
	v_fmac_f32_e32 v80, v134, v42
	v_fmac_f32_e32 v81, v134, v43
	v_fmac_f32_e32 v78, v134, v34
	v_fmac_f32_e32 v79, v134, v35
	v_fmac_f32_e32 v76, v134, v32
	v_fmac_f32_e32 v77, v134, v33
	v_fmac_f32_e32 v74, v134, v30
	v_fmac_f32_e32 v75, v134, v31
	v_fmac_f32_e32 v72, v134, v18
	v_fmac_f32_e32 v73, v134, v19
	v_fmac_f32_e32 v70, v134, v16
	v_fmac_f32_e32 v71, v134, v17
	v_fmac_f32_e32 v68, v134, v14
	v_fmac_f32_e32 v127, v134, v15
	v_fmac_f32_e32 v90, v132, v69
	v_fmac_f32_e32 v91, v132, v66
	v_fmac_f32_e32 v88, v132, v67
	v_fmac_f32_e32 v89, v132, v64
	v_fmac_f32_e32 v86, v132, v65
	v_fmac_f32_e32 v87, v132, v58
	v_fmac_f32_e32 v84, v132, v59
	v_fmac_f32_e32 v85, v132, v56
	v_fmac_f32_e32 v82, v132, v57
	v_fmac_f32_e32 v83, v132, v42
	v_fmac_f32_e32 v80, v132, v43
	v_fmac_f32_e32 v81, v132, v34
	v_fmac_f32_e32 v78, v132, v35
	v_fmac_f32_e32 v79, v132, v32
	v_fmac_f32_e32 v76, v132, v33
	v_fmac_f32_e32 v77, v132, v30
	v_fmac_f32_e32 v74, v132, v31
	v_fmac_f32_e32 v75, v132, v18
	v_fmac_f32_e32 v72, v132, v19
	v_fmac_f32_e32 v73, v132, v16
	v_fmac_f32_e32 v70, v132, v17
	v_fmac_f32_e32 v71, v132, v14
	v_fmac_f32_e32 v68, v132, v15
	v_fmac_f32_e32 v127, v132, v12
	v_fmac_f32_e32 v93, v145, v69
	v_fmac_f32_e32 v90, v145, v66
	v_fmac_f32_e32 v91, v145, v67
	v_fmac_f32_e32 v88, v145, v64
	v_fmac_f32_e32 v89, v145, v65
	v_fmac_f32_e32 v86, v145, v58
	v_fmac_f32_e32 v87, v145, v59
	v_fmac_f32_e32 v84, v145, v56
	v_fmac_f32_e32 v85, v145, v57
	v_fmac_f32_e32 v82, v145, v42
	v_fmac_f32_e32 v83, v145, v43
	v_fmac_f32_e32 v80, v145, v34
	v_fmac_f32_e32 v81, v145, v35
	v_fmac_f32_e32 v78, v145, v32
	v_fmac_f32_e32 v79, v145, v33
	v_fmac_f32_e32 v76, v145, v30
	v_fmac_f32_e32 v77, v145, v31
	v_fmac_f32_e32 v74, v145, v18
	v_fmac_f32_e32 v75, v145, v19
	v_fmac_f32_e32 v72, v145, v16
	v_fmac_f32_e32 v73, v145, v17
	v_fmac_f32_e32 v70, v145, v14
	v_fmac_f32_e32 v71, v145, v15
	v_fmac_f32_e32 v68, v145, v12
	v_fmac_f32_e32 v127, v145, v13
	v_fmac_f32_e32 v92, v143, v69
	v_fmac_f32_e32 v93, v143, v66
	v_fmac_f32_e32 v90, v143, v67
	v_fmac_f32_e32 v91, v143, v64
	v_fmac_f32_e32 v88, v143, v65
	v_fmac_f32_e32 v89, v143, v58
	v_fmac_f32_e32 v86, v143, v59
	v_fmac_f32_e32 v87, v143, v56
	v_fmac_f32_e32 v84, v143, v57
	v_fmac_f32_e32 v85, v143, v42
	v_fmac_f32_e32 v82, v143, v43
	v_fmac_f32_e32 v83, v143, v34
	v_fmac_f32_e32 v80, v143, v35
	v_fmac_f32_e32 v81, v143, v32
	v_fmac_f32_e32 v78, v143, v33
	v_fmac_f32_e32 v79, v143, v30
	v_fmac_f32_e32 v76, v143, v31
	v_fmac_f32_e32 v77, v143, v18
	v_fmac_f32_e32 v74, v143, v19
	v_fmac_f32_e32 v75, v143, v16
	v_fmac_f32_e32 v72, v143, v17
	v_fmac_f32_e32 v73, v143, v14
	v_fmac_f32_e32 v70, v143, v15
	v_fmac_f32_e32 v71, v143, v12
	v_fmac_f32_e32 v68, v143, v13
	v_fmac_f32_e32 v127, v143, v10
	v_fmac_f32_e32 v95, v141, v69
	v_fmac_f32_e32 v92, v141, v66
	v_fmac_f32_e32 v93, v141, v67
	v_fmac_f32_e32 v90, v141, v64
	v_fmac_f32_e32 v91, v141, v65
	v_fmac_f32_e32 v88, v141, v58
	v_fmac_f32_e32 v89, v141, v59
	v_fmac_f32_e32 v86, v141, v56
	v_fmac_f32_e32 v87, v141, v57
	v_fmac_f32_e32 v84, v141, v42
	v_fmac_f32_e32 v85, v141, v43
	v_fmac_f32_e32 v82, v141, v34
	v_fmac_f32_e32 v83, v141, v35
	v_fmac_f32_e32 v80, v141, v32
	v_fmac_f32_e32 v81, v141, v33
	v_fmac_f32_e32 v78, v141, v30
	v_fmac_f32_e32 v79, v141, v31
	v_fmac_f32_e32 v76, v141, v18
	v_fmac_f32_e32 v77, v141, v19
	v_fmac_f32_e32 v74, v141, v16
	v_fmac_f32_e32 v75, v141, v17
	v_fmac_f32_e32 v72, v141, v14
	v_fmac_f32_e32 v73, v141, v15
	v_fmac_f32_e32 v70, v141, v12
	v_fmac_f32_e32 v71, v141, v13
	v_fmac_f32_e32 v68, v141, v10
	v_fmac_f32_e32 v127, v141, v11
	v_fmac_f32_e32 v94, v139, v69
	v_fmac_f32_e32 v95, v139, v66
	v_fmac_f32_e32 v92, v139, v67
	v_fmac_f32_e32 v93, v139, v64
	v_fmac_f32_e32 v90, v139, v65
	v_fmac_f32_e32 v91, v139, v58
	v_fmac_f32_e32 v88, v139, v59
	v_fmac_f32_e32 v89, v139, v56
	v_fmac_f32_e32 v86, v139, v57
	v_fmac_f32_e32 v87, v139, v42
	v_fmac_f32_e32 v84, v139, v43
	v_fmac_f32_e32 v85, v139, v34
	v_fmac_f32_e32 v82, v139, v35
	v_fmac_f32_e32 v83, v139, v32
	v_fmac_f32_e32 v80, v139, v33
	v_fmac_f32_e32 v81, v139, v30
	v_fmac_f32_e32 v78, v139, v31
	v_fmac_f32_e32 v79, v139, v18
	v_fmac_f32_e32 v76, v139, v19
	v_fmac_f32_e32 v77, v139, v16
	v_fmac_f32_e32 v74, v139, v17
	v_fmac_f32_e32 v75, v139, v14
	v_fmac_f32_e32 v72, v139, v15
	v_fmac_f32_e32 v73, v139, v12
	v_fmac_f32_e32 v70, v139, v13
	v_fmac_f32_e32 v71, v139, v10
	v_fmac_f32_e32 v68, v139, v11
	v_fmac_f32_e32 v127, v139, v8
	v_fmac_f32_e32 v150, v137, v69
	v_fmac_f32_e32 v94, v137, v66
	v_fmac_f32_e32 v95, v137, v67
	v_fmac_f32_e32 v92, v137, v64
	v_fmac_f32_e32 v93, v137, v65
	v_fmac_f32_e32 v90, v137, v58
	v_fmac_f32_e32 v91, v137, v59
	v_fmac_f32_e32 v88, v137, v56
	v_fmac_f32_e32 v89, v137, v57
	v_fmac_f32_e32 v86, v137, v42
	v_fmac_f32_e32 v87, v137, v43
	v_fmac_f32_e32 v84, v137, v34
	v_fmac_f32_e32 v85, v137, v35
	v_fmac_f32_e32 v82, v137, v32
	v_fmac_f32_e32 v83, v137, v33
	v_fmac_f32_e32 v80, v137, v30
	v_fmac_f32_e32 v81, v137, v31
	v_fmac_f32_e32 v78, v137, v18
	v_fmac_f32_e32 v79, v137, v19
	v_fmac_f32_e32 v76, v137, v16
	v_fmac_f32_e32 v77, v137, v17
	v_fmac_f32_e32 v74, v137, v14
	v_fmac_f32_e32 v75, v137, v15
	v_fmac_f32_e32 v72, v137, v12
	v_fmac_f32_e32 v73, v137, v13
	v_fmac_f32_e32 v70, v137, v10
	v_fmac_f32_e32 v71, v137, v11
	v_fmac_f32_e32 v68, v137, v8
	v_fmac_f32_e32 v127, v137, v9
	v_fmac_f32_e32 v148, v133, v69
	v_fmac_f32_e32 v149, v135, v69
	v_fmac_f32_e32 v150, v135, v66
	v_fmac_f32_e32 v94, v135, v67
	v_fmac_f32_e32 v95, v135, v64
	v_fmac_f32_e32 v92, v135, v65
	v_fmac_f32_e32 v93, v135, v58
	v_fmac_f32_e32 v90, v135, v59
	v_fmac_f32_e32 v91, v135, v56
	v_fmac_f32_e32 v88, v135, v57
	v_fmac_f32_e32 v89, v135, v42
	v_fmac_f32_e32 v86, v135, v43
	v_fmac_f32_e32 v87, v135, v34
	v_fmac_f32_e32 v84, v135, v35
	v_fmac_f32_e32 v85, v135, v32
	v_fmac_f32_e32 v82, v135, v33
	v_fmac_f32_e32 v83, v135, v30
	v_fmac_f32_e32 v80, v135, v31
	v_fmac_f32_e32 v81, v135, v18
	v_fmac_f32_e32 v78, v135, v19
	v_fmac_f32_e32 v79, v135, v16
	v_fmac_f32_e32 v76, v135, v17
	v_fmac_f32_e32 v77, v135, v14
	v_fmac_f32_e32 v74, v135, v15
	v_fmac_f32_e32 v75, v135, v12
	v_fmac_f32_e32 v72, v135, v13
	v_fmac_f32_e32 v73, v135, v10
	v_fmac_f32_e32 v70, v135, v11
	v_fmac_f32_e32 v71, v135, v8
	v_fmac_f32_e32 v68, v135, v9
	v_fmac_f32_e32 v127, v135, v6
	v_fmac_f32_e32 v149, v133, v66
	v_fmac_f32_e32 v150, v133, v67
	v_fmac_f32_e32 v94, v133, v64
	v_fmac_f32_e32 v95, v133, v65
	v_fmac_f32_e32 v92, v133, v58
	v_fmac_f32_e32 v93, v133, v59
	v_fmac_f32_e32 v90, v133, v56
	v_fmac_f32_e32 v91, v133, v57
	v_fmac_f32_e32 v88, v133, v42
	v_fmac_f32_e32 v89, v133, v43
	v_fmac_f32_e32 v86, v133, v34
	v_fmac_f32_e32 v87, v133, v35
	v_fmac_f32_e32 v84, v133, v32
	v_fmac_f32_e32 v85, v133, v33
	v_fmac_f32_e32 v82, v133, v30
	v_fmac_f32_e32 v83, v133, v31
	v_fmac_f32_e32 v80, v133, v18
	v_fmac_f32_e32 v81, v133, v19
	v_fmac_f32_e32 v78, v133, v16
	v_fmac_f32_e32 v79, v133, v17
	v_fmac_f32_e32 v76, v133, v14
	v_fmac_f32_e32 v77, v133, v15
	v_fmac_f32_e32 v74, v133, v12
	v_fmac_f32_e32 v75, v133, v13
	v_fmac_f32_e32 v72, v133, v10
	v_fmac_f32_e32 v73, v133, v11
	v_fmac_f32_e32 v70, v133, v8
	v_fmac_f32_e32 v71, v133, v9
	v_fmac_f32_e32 v68, v133, v6
	v_fmac_f32_e32 v127, v133, v7
	ds_write2st64_b32 v45, v147, v148 offset1:2
	ds_write2st64_b32 v45, v149, v150 offset0:4 offset1:6
	ds_write2st64_b32 v45, v94, v95 offset0:8 offset1:10
	ds_write2st64_b32 v45, v92, v93 offset0:12 offset1:14
	ds_write2st64_b32 v45, v90, v91 offset0:16 offset1:18
	ds_write2st64_b32 v45, v88, v89 offset0:20 offset1:22
	ds_write2st64_b32 v45, v86, v87 offset0:24 offset1:26
	ds_write2st64_b32 v45, v84, v85 offset0:28 offset1:30
	ds_write2st64_b32 v45, v82, v83 offset0:32 offset1:34
	ds_write2st64_b32 v45, v80, v81 offset0:36 offset1:38
	ds_write2st64_b32 v45, v78, v79 offset0:40 offset1:42
	ds_write2st64_b32 v45, v76, v77 offset0:44 offset1:46
	ds_write2st64_b32 v45, v74, v75 offset0:48 offset1:50
	ds_write2st64_b32 v45, v72, v73 offset0:52 offset1:54
	ds_write2st64_b32 v45, v70, v71 offset0:56 offset1:58
	ds_write2st64_b32 v45, v68, v127 offset0:60 offset1:62
	s_waitcnt lgkmcnt(0)
	s_barrier
	ds_read_b128 v[30:33], v63
	ds_read_b128 v[56:59], v63 offset:16
	v_lshl_add_u64 v[8:9], v[24:25], 0, v[4:5]
	v_lshl_add_u64 v[10:11], v[26:27], 0, v[4:5]
	s_waitcnt lgkmcnt(1)
	v_add_f32_e32 v6, 0, v30
	v_add_f32_e32 v6, v31, v6
	v_add_f32_e32 v6, v32, v6
	v_add_f32_e32 v6, v33, v6
	s_waitcnt lgkmcnt(0)
	v_add_f32_e32 v6, v56, v6
	v_add_f32_e32 v6, v57, v6
	v_add_f32_e32 v6, v58, v6
	v_add_f32_e32 v6, v59, v6
	s_nop 0
	s_waitcnt lgkmcnt(0)
	v_add_f32_dpp v6, v6, v6 quad_perm:[1,0,3,2] row_mask:0xf bank_mask:0xf
	s_nop 0
	s_waitcnt lgkmcnt(0)
	v_add_f32_dpp v6, v6, v6 quad_perm:[2,3,0,1] row_mask:0xf bank_mask:0xf
	ds_bpermute_b32 v7, v104, v6
	s_waitcnt lgkmcnt(0)
	v_add_f32_e32 v12, v6, v7
	ds_bpermute_b32 v13, v105, v12
	global_load_dwordx4 v[16:19], v[8:9], off
	global_load_dwordx4 v[4:7], v[10:11], off
	s_waitcnt lgkmcnt(0)
	v_add_f32_e32 v12, v12, v13
	v_fmamk_f32 v31, v12, 0xbc000000, v31
	v_fmamk_f32 v30, v12, 0xbc000000, v30
	v_mul_f32_e32 v13, v31, v31
	v_fmac_f32_e32 v13, v30, v30
	v_fmamk_f32 v32, v12, 0xbc000000, v32
	v_fmac_f32_e32 v13, v32, v32
	v_fmac_f32_e32 v33, 0xbc000000, v12
	v_fmac_f32_e32 v13, v33, v33
	v_fmamk_f32 v34, v12, 0xbc000000, v56
	v_fmac_f32_e32 v13, v34, v34
	v_fmamk_f32 v35, v12, 0xbc000000, v57
	v_fmac_f32_e32 v13, v35, v35
	v_fmamk_f32 v42, v12, 0xbc000000, v58
	v_fmac_f32_e32 v13, v42, v42
	v_fmac_f32_e32 v59, 0xbc000000, v12
	v_fmac_f32_e32 v13, v59, v59
	ds_bpermute_b32 v12, v102, v13
	s_waitcnt lgkmcnt(0)
	v_add_f32_e32 v43, v13, v12
	global_load_dwordx4 v[12:15], v[8:9], off offset:16
	s_nop 0
	global_load_dwordx4 v[8:11], v[10:11], off offset:16
	s_nop 0
	s_waitcnt lgkmcnt(0)
	v_add_f32_dpp v43, v43, v43 quad_perm:[2,3,0,1] row_mask:0xf bank_mask:0xf
	s_nop 0
	s_waitcnt lgkmcnt(0)
	v_add_f32_dpp v43, v43, v43 row_half_mirror row_mask:0xf bank_mask:0xf
	s_nop 0
	s_waitcnt lgkmcnt(0)
	v_add_f32_dpp v43, v43, v43 row_mirror row_mask:0xf bank_mask:0xf
	v_fmamk_f32 v43, v43, 0x3c000000, v217
	v_mul_f32_e32 v56, 0x4f800000, v43
	v_cmp_gt_f32_e32 vcc, s10, v43
	s_nop 1
	v_cndmask_b32_e32 v43, v43, v56, vcc
	v_sqrt_f32_e32 v56, v43
	s_nop 0
	v_add_u32_e32 v57, -1, v56
	v_fma_f32 v58, -v57, v56, v43
	v_cmp_ge_f32_e64 s[4:5], 0, v58
	v_add_u32_e32 v58, 1, v56
	s_nop 0
	v_cndmask_b32_e64 v57, v56, v57, s[4:5]
	v_fma_f32 v56, -v58, v56, v43
	v_cmp_lt_f32_e64 s[4:5], 0, v56
	s_nop 1
	v_cndmask_b32_e64 v56, v57, v58, s[4:5]
	v_mul_f32_e32 v57, 0x37800000, v56
	v_cndmask_b32_e32 v56, v56, v57, vcc
	v_cmp_class_f32_e32 vcc, v43, v218
	s_nop 1
	v_cndmask_b32_e32 v43, v56, v43, vcc
	v_div_scale_f32 v56, s[4:5], v43, v43, 1.0
	v_rcp_f32_e32 v57, v56
	s_nop 0
	v_fma_f32 v58, -v56, v57, 1.0
	v_fmac_f32_e32 v57, v58, v57
	v_div_scale_f32 v58, vcc, 1.0, v43, 1.0
	v_mul_f32_e32 v64, v58, v57
	v_fma_f32 v65, -v56, v64, v58
	v_fmac_f32_e32 v64, v65, v57
	v_fma_f32 v56, -v56, v64, v58
	v_div_fmas_f32 v56, v56, v57, v64
	v_div_fixup_f32 v43, v56, v43, 1.0
	v_mul_f32_e32 v30, v30, v43
	v_mul_f32_e32 v31, v31, v43
	v_mul_f32_e32 v32, v32, v43
	s_waitcnt vmcnt(2)
	v_fma_f32 v30, v16, v30, v4
	v_fma_f32 v31, v17, v31, v5
	v_fma_f32 v32, v18, v32, v6
	v_mul_f32_e32 v56, 0xbfb8aa3b, v30
	v_mul_f32_e32 v57, 0xbfb8aa3b, v31
	v_mul_f32_e32 v58, 0xbfb8aa3b, v32
	v_exp_f32_e32 v56, v56
	v_exp_f32_e32 v57, v57
	v_exp_f32_e32 v58, v58
	v_mul_f32_e32 v33, v33, v43
	v_fma_f32 v33, v19, v33, v7
	v_add_f32_e32 v56, 1.0, v56
	v_add_f32_e32 v57, 1.0, v57
	v_add_f32_e32 v58, 1.0, v58
	v_mul_f32_e32 v64, 0xbfb8aa3b, v33
	v_rcp_f32_e32 v56, v56
	v_rcp_f32_e32 v57, v57
	v_rcp_f32_e32 v58, v58
	v_exp_f32_e32 v64, v64
	v_mul_f32_e32 v34, v34, v43
	v_mul_f32_e32 v35, v35, v43
	s_waitcnt vmcnt(0)
	v_fma_f32 v34, v12, v34, v8
	v_fma_f32 v35, v13, v35, v9
	v_mul_f32_e32 v30, v30, v56
	v_mul_f32_e32 v31, v31, v57
	v_mul_f32_e32 v32, v32, v58
	v_add_f32_e32 v56, 1.0, v64
	v_mul_f32_e32 v57, 0xbfb8aa3b, v34
	v_mul_f32_e32 v58, 0xbfb8aa3b, v35
	v_rcp_f32_e32 v56, v56
	v_exp_f32_e32 v57, v57
	v_exp_f32_e32 v58, v58
	v_mul_f32_e32 v42, v42, v43
	v_mul_f32_e32 v43, v59, v43
	v_fma_f32 v42, v14, v42, v10
	v_fma_f32 v43, v15, v43, v11
	v_mul_f32_e32 v33, v33, v56
	v_add_f32_e32 v56, 1.0, v57
	v_add_f32_e32 v57, 1.0, v58
	v_mul_f32_e32 v58, 0xbfb8aa3b, v42
	v_mul_f32_e32 v59, 0xbfb8aa3b, v43
	v_exp_f32_e32 v58, v58
	v_exp_f32_e32 v59, v59
	v_rcp_f32_e32 v56, v56
	v_rcp_f32_e32 v57, v57
	v_add_f32_e32 v58, 1.0, v58
	v_add_f32_e32 v59, 1.0, v59
	v_rcp_f32_e32 v58, v58
	v_rcp_f32_e32 v59, v59
	v_mul_f32_e32 v34, v34, v56
	v_mul_f32_e32 v35, v35, v57
	v_mul_f32_e32 v42, v42, v58
	v_mul_f32_e32 v43, v43, v59
	v_cvt_pk_bf16_f32 v30, v30, v31
	v_cvt_pk_bf16_f32 v31, v32, v33
	v_cvt_pk_bf16_f32 v32, v34, v35
	v_cvt_pk_bf16_f32 v33, v42, v43
	ds_read_b128 v[56:59], v112
	ds_read_b128 v[64:67], v112 offset:16
	s_waitcnt lgkmcnt(1)
	v_add_f32_e32 v34, 0, v56
	v_add_f32_e32 v34, v57, v34
	v_add_f32_e32 v34, v58, v34
	v_add_f32_e32 v34, v59, v34
	s_waitcnt lgkmcnt(0)
	v_add_f32_e32 v34, v64, v34
	v_add_f32_e32 v34, v65, v34
	v_add_f32_e32 v34, v66, v34
	v_add_f32_e32 v34, v67, v34
	s_nop 0
	s_waitcnt lgkmcnt(0)
	v_add_f32_dpp v34, v34, v34 quad_perm:[1,0,3,2] row_mask:0xf bank_mask:0xf
	s_nop 0
	s_waitcnt lgkmcnt(0)
	v_add_f32_dpp v34, v34, v34 quad_perm:[2,3,0,1] row_mask:0xf bank_mask:0xf
	s_nop 0
	s_waitcnt lgkmcnt(0)
	v_add_f32_dpp v34, v34, v34 row_half_mirror row_mask:0xf bank_mask:0xf
	s_nop 0
	s_waitcnt lgkmcnt(0)
	v_add_f32_dpp v34, v34, v34 row_mirror row_mask:0xf bank_mask:0xf
	v_fmamk_f32 v43, v34, 0xbc000000, v57
	v_fmamk_f32 v42, v34, 0xbc000000, v56
	v_mul_f32_e32 v35, v43, v43
	v_fmac_f32_e32 v35, v42, v42
	v_fmamk_f32 v56, v34, 0xbc000000, v58
	v_fmac_f32_e32 v35, v56, v56
	v_fmac_f32_e32 v59, 0xbc000000, v34
	v_fmac_f32_e32 v35, v59, v59
	v_fmamk_f32 v57, v34, 0xbc000000, v64
	v_fmac_f32_e32 v35, v57, v57
	v_fmamk_f32 v58, v34, 0xbc000000, v65
	v_fmac_f32_e32 v35, v58, v58
	v_fmamk_f32 v64, v34, 0xbc000000, v66
	v_fmac_f32_e32 v35, v64, v64
	v_fmac_f32_e32 v67, 0xbc000000, v34
	v_fmac_f32_e32 v35, v67, v67
	ds_bpermute_b32 v34, v102, v35
	s_waitcnt lgkmcnt(0)
	v_add_f32_e32 v34, v35, v34
	s_nop 0
	s_waitcnt lgkmcnt(0)
	v_add_f32_dpp v34, v34, v34 quad_perm:[2,3,0,1] row_mask:0xf bank_mask:0xf
	ds_bpermute_b32 v35, v104, v34
	s_waitcnt lgkmcnt(0)
	v_add_f32_e32 v35, v34, v35
	ds_bpermute_b32 v65, v105, v35
	v_add_u32_e32 v34, s87, v101
	s_waitcnt lgkmcnt(0)
	v_add_f32_e32 v35, v35, v65
	v_fmamk_f32 v35, v35, 0x3c000000, v217
	v_mul_f32_e32 v65, 0x4f800000, v35
	v_cmp_gt_f32_e32 vcc, s10, v35
	s_nop 1
	v_cndmask_b32_e32 v65, v35, v65, vcc
	v_sqrt_f32_e32 v66, v65
	v_ashrrev_i32_e32 v35, 31, v34
	v_lshlrev_b64 v[34:35], 12, v[34:35]
	v_lshl_add_u64 v[34:35], s[6:7], 0, v[34:35]
	v_add_u32_e32 v68, -1, v66
	v_fma_f32 v69, -v68, v66, v65
	v_cmp_ge_f32_e64 s[4:5], 0, v69
	v_add_u32_e32 v69, 1, v66
	v_lshl_add_u64 v[34:35], v[34:35], 0, v[28:29]
	v_cndmask_b32_e64 v68, v66, v68, s[4:5]
	v_fma_f32 v66, -v69, v66, v65
	v_cmp_lt_f32_e64 s[4:5], 0, v66
	v_lshl_add_u64 v[34:35], v[34:35], 0, v[2:3]
	s_nop 0
	v_cndmask_b32_e64 v66, v68, v69, s[4:5]
	v_mul_f32_e32 v68, 0x37800000, v66
	v_cndmask_b32_e32 v66, v66, v68, vcc
	v_cmp_class_f32_e32 vcc, v65, v218
	s_nop 1
	v_cndmask_b32_e32 v65, v66, v65, vcc
	v_div_scale_f32 v66, s[4:5], v65, v65, 1.0
	v_rcp_f32_e32 v68, v66
	s_nop 0
	v_fma_f32 v69, -v66, v68, 1.0
	v_fmac_f32_e32 v68, v69, v68
	v_div_scale_f32 v69, vcc, 1.0, v65, 1.0
	v_mul_f32_e32 v70, v69, v68
	v_fma_f32 v71, -v66, v70, v69
	v_fmac_f32_e32 v70, v71, v68
	v_fma_f32 v66, -v66, v70, v69
	v_div_fmas_f32 v66, v66, v68, v70
	v_add_co_u32_e32 v34, vcc, s11, v34
	v_div_fixup_f32 v65, v66, v65, 1.0
	s_nop 0
	v_addc_co_u32_e32 v35, vcc, 0, v35, vcc
	global_store_dwordx4 v[34:35], v[30:33], off offset:2048
	v_mul_f32_e32 v42, v42, v65
	v_fma_f32 v42, v16, v42, v4
	v_mul_f32_e32 v31, v43, v65
	v_mul_f32_e32 v33, v56, v65
	v_fma_f32 v31, v17, v31, v5
	v_fma_f32 v33, v18, v33, v6
	v_mul_f32_e32 v32, 0xbfb8aa3b, v31
	v_mul_f32_e32 v34, 0xbfb8aa3b, v33
	v_exp_f32_e32 v32, v32
	v_exp_f32_e32 v34, v34
	v_mul_f32_e32 v66, 0xbfb8aa3b, v42
	v_exp_f32_e32 v66, v66
	v_mul_f32_e32 v35, v59, v65
	v_fma_f32 v35, v19, v35, v7
	v_add_f32_e32 v32, 1.0, v32
	v_add_f32_e32 v34, 1.0, v34
	v_mul_f32_e32 v43, 0xbfb8aa3b, v35
	v_rcp_f32_e32 v32, v32
	v_rcp_f32_e32 v34, v34
	v_exp_f32_e32 v43, v43
	v_add_f32_e32 v30, 1.0, v66
	v_rcp_f32_e32 v30, v30
	v_mul_f32_e32 v31, v31, v32
	v_mul_f32_e32 v32, v33, v34
	v_add_f32_e32 v33, 1.0, v43
	v_mul_f32_e32 v34, v57, v65
	v_mul_f32_e32 v43, v58, v65
	v_fma_f32 v34, v12, v34, v8
	v_fma_f32 v43, v13, v43, v9
	v_mul_f32_e32 v30, v42, v30
	v_mul_f32_e32 v42, 0xbfb8aa3b, v34
	v_mul_f32_e32 v56, 0xbfb8aa3b, v43
	v_rcp_f32_e32 v33, v33
	v_exp_f32_e32 v42, v42
	v_exp_f32_e32 v56, v56
	v_mul_f32_e32 v58, v67, v65
	v_mul_f32_e32 v33, v35, v33
	v_add_f32_e32 v35, 1.0, v42
	v_add_f32_e32 v42, 1.0, v56
	v_mul_f32_e32 v56, v64, v65
	v_fma_f32 v56, v14, v56, v10
	v_fma_f32 v58, v15, v58, v11
	v_mul_f32_e32 v57, 0xbfb8aa3b, v56
	v_mul_f32_e32 v59, 0xbfb8aa3b, v58
	v_exp_f32_e32 v57, v57
	v_exp_f32_e32 v59, v59
	v_rcp_f32_e32 v35, v35
	v_rcp_f32_e32 v42, v42
	v_add_f32_e32 v57, 1.0, v57
	v_add_f32_e32 v59, 1.0, v59
	v_rcp_f32_e32 v57, v57
	v_rcp_f32_e32 v59, v59
	v_mul_f32_e32 v34, v34, v35
	v_mul_f32_e32 v35, v43, v42
	v_mul_f32_e32 v42, v56, v57
	v_mul_f32_e32 v43, v58, v59
	v_cvt_pk_bf16_f32 v30, v30, v31
	v_cvt_pk_bf16_f32 v31, v32, v33
	v_cvt_pk_bf16_f32 v32, v34, v35
	v_cvt_pk_bf16_f32 v33, v42, v43
	ds_read_b128 v[56:59], v113
	ds_read_b128 v[64:67], v113 offset:16
	s_waitcnt lgkmcnt(1)
	v_add_f32_e32 v34, 0, v56
	v_add_f32_e32 v34, v57, v34
	v_add_f32_e32 v34, v58, v34
	v_add_f32_e32 v34, v59, v34
	s_waitcnt lgkmcnt(0)
	v_add_f32_e32 v34, v64, v34
	v_add_f32_e32 v34, v65, v34
	v_add_f32_e32 v34, v66, v34
	v_add_f32_e32 v34, v67, v34
	s_nop 0
	s_waitcnt lgkmcnt(0)
	v_add_f32_dpp v34, v34, v34 quad_perm:[1,0,3,2] row_mask:0xf bank_mask:0xf
	s_nop 0
	s_waitcnt lgkmcnt(0)
	v_add_f32_dpp v34, v34, v34 quad_perm:[2,3,0,1] row_mask:0xf bank_mask:0xf
	s_nop 0
	s_waitcnt lgkmcnt(0)
	v_add_f32_dpp v34, v34, v34 row_half_mirror row_mask:0xf bank_mask:0xf
	s_nop 0
	s_waitcnt lgkmcnt(0)
	v_add_f32_dpp v34, v34, v34 row_mirror row_mask:0xf bank_mask:0xf
	v_fmamk_f32 v43, v34, 0xbc000000, v57
	v_fmamk_f32 v42, v34, 0xbc000000, v56
	v_mul_f32_e32 v35, v43, v43
	v_fmac_f32_e32 v35, v42, v42
	v_fmamk_f32 v56, v34, 0xbc000000, v58
	v_fmac_f32_e32 v35, v56, v56
	v_fmac_f32_e32 v59, 0xbc000000, v34
	v_fmac_f32_e32 v35, v59, v59
	v_fmamk_f32 v57, v34, 0xbc000000, v64
	v_fmac_f32_e32 v35, v57, v57
	v_fmamk_f32 v58, v34, 0xbc000000, v65
	v_fmac_f32_e32 v35, v58, v58
	v_fmamk_f32 v64, v34, 0xbc000000, v66
	v_fmac_f32_e32 v35, v64, v64
	v_fmac_f32_e32 v67, 0xbc000000, v34
	v_fmac_f32_e32 v35, v67, v67
	ds_bpermute_b32 v34, v102, v35
	s_waitcnt lgkmcnt(0)
	v_add_f32_e32 v34, v35, v34
	s_nop 0
	s_waitcnt lgkmcnt(0)
	v_add_f32_dpp v34, v34, v34 quad_perm:[2,3,0,1] row_mask:0xf bank_mask:0xf
	s_nop 0
	s_waitcnt lgkmcnt(0)
	v_add_f32_dpp v34, v34, v34 row_half_mirror row_mask:0xf bank_mask:0xf
	s_nop 0
	s_waitcnt lgkmcnt(0)
	v_add_f32_dpp v34, v34, v34 row_mirror row_mask:0xf bank_mask:0xf
	v_fmamk_f32 v34, v34, 0x3c000000, v217
	v_mul_f32_e32 v35, 0x4f800000, v34
	v_cmp_gt_f32_e32 vcc, s10, v34
	s_nop 1
	v_cndmask_b32_e32 v65, v34, v35, vcc
	v_sqrt_f32_e32 v66, v65
	v_add_u32_e32 v34, s87, v47
	v_ashrrev_i32_e32 v35, 31, v34
	v_lshlrev_b64 v[34:35], 12, v[34:35]
	v_add_u32_e32 v68, -1, v66
	v_fma_f32 v69, -v68, v66, v65
	v_cmp_ge_f32_e64 s[4:5], 0, v69
	v_add_u32_e32 v69, 1, v66
	v_lshl_add_u64 v[34:35], s[6:7], 0, v[34:35]
	v_cndmask_b32_e64 v68, v66, v68, s[4:5]
	v_fma_f32 v66, -v69, v66, v65
	v_cmp_lt_f32_e64 s[4:5], 0, v66
	v_lshl_add_u64 v[34:35], v[34:35], 0, v[28:29]
	v_lshl_add_u64 v[34:35], v[34:35], 0, v[2:3]
	v_cndmask_b32_e64 v66, v68, v69, s[4:5]
	v_mul_f32_e32 v68, 0x37800000, v66
	v_cndmask_b32_e32 v66, v66, v68, vcc
	v_cmp_class_f32_e32 vcc, v65, v218
	s_nop 1
	v_cndmask_b32_e32 v65, v66, v65, vcc
	v_div_scale_f32 v66, s[4:5], v65, v65, 1.0
	v_rcp_f32_e32 v68, v66
	s_nop 0
	v_fma_f32 v69, -v66, v68, 1.0
	v_fmac_f32_e32 v68, v69, v68
	v_div_scale_f32 v69, vcc, 1.0, v65, 1.0
	v_mul_f32_e32 v70, v69, v68
	v_fma_f32 v71, -v66, v70, v69
	v_fmac_f32_e32 v70, v71, v68
	v_fma_f32 v66, -v66, v70, v69
	v_div_fmas_f32 v66, v66, v68, v70
	v_add_co_u32_e32 v34, vcc, s11, v34
	v_div_fixup_f32 v65, v66, v65, 1.0
	s_nop 0
	v_addc_co_u32_e32 v35, vcc, 0, v35, vcc
	global_store_dwordx4 v[34:35], v[30:33], off offset:2048
	v_mul_f32_e32 v42, v42, v65
	v_fma_f32 v42, v16, v42, v4
	v_mul_f32_e32 v31, v43, v65
	v_mul_f32_e32 v33, v56, v65
	v_fma_f32 v31, v17, v31, v5
	v_fma_f32 v33, v18, v33, v6
	v_mul_f32_e32 v32, 0xbfb8aa3b, v31
	v_mul_f32_e32 v34, 0xbfb8aa3b, v33
	v_exp_f32_e32 v32, v32
	v_exp_f32_e32 v34, v34
	v_mul_f32_e32 v66, 0xbfb8aa3b, v42
	v_exp_f32_e32 v66, v66
	v_mul_f32_e32 v35, v59, v65
	v_fma_f32 v35, v19, v35, v7
	v_add_f32_e32 v32, 1.0, v32
	v_add_f32_e32 v34, 1.0, v34
	v_mul_f32_e32 v43, 0xbfb8aa3b, v35
	v_rcp_f32_e32 v32, v32
	v_rcp_f32_e32 v34, v34
	v_exp_f32_e32 v43, v43
	v_add_f32_e32 v30, 1.0, v66
	v_rcp_f32_e32 v30, v30
	v_mul_f32_e32 v31, v31, v32
	v_mul_f32_e32 v32, v33, v34
	v_add_f32_e32 v33, 1.0, v43
	v_mul_f32_e32 v34, v57, v65
	v_mul_f32_e32 v43, v58, v65
	v_fma_f32 v34, v12, v34, v8
	v_fma_f32 v43, v13, v43, v9
	v_mul_f32_e32 v30, v42, v30
	v_mul_f32_e32 v42, 0xbfb8aa3b, v34
	v_mul_f32_e32 v56, 0xbfb8aa3b, v43
	v_rcp_f32_e32 v33, v33
	v_exp_f32_e32 v42, v42
	v_exp_f32_e32 v56, v56
	v_mul_f32_e32 v58, v67, v65
	v_mul_f32_e32 v33, v35, v33
	v_add_f32_e32 v35, 1.0, v42
	v_add_f32_e32 v42, 1.0, v56
	v_mul_f32_e32 v56, v64, v65
	v_fma_f32 v56, v14, v56, v10
	v_fma_f32 v58, v15, v58, v11
	v_mul_f32_e32 v57, 0xbfb8aa3b, v56
	v_mul_f32_e32 v59, 0xbfb8aa3b, v58
	v_exp_f32_e32 v57, v57
	v_exp_f32_e32 v59, v59
	v_rcp_f32_e32 v35, v35
	v_rcp_f32_e32 v42, v42
	v_add_f32_e32 v57, 1.0, v57
	v_add_f32_e32 v59, 1.0, v59
	v_rcp_f32_e32 v57, v57
	v_rcp_f32_e32 v59, v59
	v_mul_f32_e32 v34, v34, v35
	v_mul_f32_e32 v35, v43, v42
	v_mul_f32_e32 v42, v56, v57
	v_mul_f32_e32 v43, v58, v59
	v_cvt_pk_bf16_f32 v30, v30, v31
	v_cvt_pk_bf16_f32 v31, v32, v33
	v_cvt_pk_bf16_f32 v32, v34, v35
	v_cvt_pk_bf16_f32 v33, v42, v43
	ds_read_b128 v[56:59], v114
	ds_read_b128 v[64:67], v114 offset:16
	s_waitcnt lgkmcnt(1)
	v_add_f32_e32 v34, 0, v56
	v_add_f32_e32 v34, v57, v34
	v_add_f32_e32 v34, v58, v34
	v_add_f32_e32 v34, v59, v34
	s_waitcnt lgkmcnt(0)
	v_add_f32_e32 v34, v64, v34
	v_add_f32_e32 v34, v65, v34
	v_add_f32_e32 v34, v66, v34
	v_add_f32_e32 v34, v67, v34
	s_nop 0
	s_waitcnt lgkmcnt(0)
	v_add_f32_dpp v34, v34, v34 quad_perm:[1,0,3,2] row_mask:0xf bank_mask:0xf
	s_nop 0
	s_waitcnt lgkmcnt(0)
	v_add_f32_dpp v34, v34, v34 quad_perm:[2,3,0,1] row_mask:0xf bank_mask:0xf
	s_nop 0
	s_waitcnt lgkmcnt(0)
	v_add_f32_dpp v34, v34, v34 row_half_mirror row_mask:0xf bank_mask:0xf
	s_nop 0
	s_waitcnt lgkmcnt(0)
	v_add_f32_dpp v34, v34, v34 row_mirror row_mask:0xf bank_mask:0xf
	v_fmamk_f32 v43, v34, 0xbc000000, v57
	v_fmamk_f32 v42, v34, 0xbc000000, v56
	v_mul_f32_e32 v35, v43, v43
	v_fmac_f32_e32 v35, v42, v42
	v_fmamk_f32 v56, v34, 0xbc000000, v58
	v_fmac_f32_e32 v35, v56, v56
	v_fmac_f32_e32 v59, 0xbc000000, v34
	v_fmac_f32_e32 v35, v59, v59
	v_fmamk_f32 v57, v34, 0xbc000000, v64
	v_fmac_f32_e32 v35, v57, v57
	v_fmamk_f32 v58, v34, 0xbc000000, v65
	v_fmac_f32_e32 v35, v58, v58
	v_fmamk_f32 v64, v34, 0xbc000000, v66
	v_fmac_f32_e32 v35, v64, v64
	v_fmac_f32_e32 v67, 0xbc000000, v34
	v_fmac_f32_e32 v35, v67, v67
	ds_bpermute_b32 v34, v102, v35
	s_waitcnt lgkmcnt(0)
	v_add_f32_e32 v34, v35, v34
	s_nop 0
	s_waitcnt lgkmcnt(0)
	v_add_f32_dpp v34, v34, v34 quad_perm:[2,3,0,1] row_mask:0xf bank_mask:0xf
	s_nop 0
	s_waitcnt lgkmcnt(0)
	v_add_f32_dpp v34, v34, v34 row_half_mirror row_mask:0xf bank_mask:0xf
	s_nop 0
	s_waitcnt lgkmcnt(0)
	v_add_f32_dpp v34, v34, v34 row_mirror row_mask:0xf bank_mask:0xf
	v_fmamk_f32 v34, v34, 0x3c000000, v217
	v_mul_f32_e32 v35, 0x4f800000, v34
	v_cmp_gt_f32_e32 vcc, s10, v34
	s_nop 1
	v_cndmask_b32_e32 v65, v34, v35, vcc
	v_sqrt_f32_e32 v66, v65
	v_add_u32_e32 v34, s87, v51
	v_ashrrev_i32_e32 v35, 31, v34
	v_lshlrev_b64 v[34:35], 12, v[34:35]
	v_add_u32_e32 v68, -1, v66
	v_fma_f32 v69, -v68, v66, v65
	v_cmp_ge_f32_e64 s[4:5], 0, v69
	v_add_u32_e32 v69, 1, v66
	v_lshl_add_u64 v[34:35], s[6:7], 0, v[34:35]
	v_cndmask_b32_e64 v68, v66, v68, s[4:5]
	v_fma_f32 v66, -v69, v66, v65
	v_cmp_lt_f32_e64 s[4:5], 0, v66
	v_lshl_add_u64 v[34:35], v[34:35], 0, v[28:29]
	v_lshl_add_u64 v[34:35], v[34:35], 0, v[2:3]
	v_cndmask_b32_e64 v66, v68, v69, s[4:5]
	v_mul_f32_e32 v68, 0x37800000, v66
	v_cndmask_b32_e32 v66, v66, v68, vcc
	v_cmp_class_f32_e32 vcc, v65, v218
	s_nop 1
	v_cndmask_b32_e32 v65, v66, v65, vcc
	v_div_scale_f32 v66, s[4:5], v65, v65, 1.0
	v_rcp_f32_e32 v68, v66
	s_nop 0
	v_fma_f32 v69, -v66, v68, 1.0
	v_fmac_f32_e32 v68, v69, v68
	v_div_scale_f32 v69, vcc, 1.0, v65, 1.0
	v_mul_f32_e32 v70, v69, v68
	v_fma_f32 v71, -v66, v70, v69
	v_fmac_f32_e32 v70, v71, v68
	v_fma_f32 v66, -v66, v70, v69
	v_div_fmas_f32 v66, v66, v68, v70
	v_add_co_u32_e32 v34, vcc, s11, v34
	v_div_fixup_f32 v65, v66, v65, 1.0
	s_nop 0
	v_addc_co_u32_e32 v35, vcc, 0, v35, vcc
	global_store_dwordx4 v[34:35], v[30:33], off offset:2048
	v_mul_f32_e32 v42, v42, v65
	v_fma_f32 v4, v16, v42, v4
	v_mul_f32_e32 v30, v43, v65
	v_fma_f32 v5, v17, v30, v5
	v_mul_f32_e32 v17, 0xbfb8aa3b, v5
	v_exp_f32_e32 v17, v17
	v_mul_f32_e32 v16, 0xbfb8aa3b, v4
	v_exp_f32_e32 v16, v16
	v_mul_f32_e32 v30, v56, v65
	v_add_f32_e32 v17, 1.0, v17
	v_fma_f32 v6, v18, v30, v6
	v_rcp_f32_e32 v17, v17
	v_mul_f32_e32 v30, v59, v65
	v_fmac_f32_e32 v7, v19, v30
	v_add_f32_e32 v16, 1.0, v16
	v_mul_f32_e32 v19, 0xbfb8aa3b, v7
	v_rcp_f32_e32 v16, v16
	v_exp_f32_e32 v19, v19
	v_mul_f32_e32 v5, v5, v17
	v_mul_f32_e32 v17, v57, v65
	v_fma_f32 v8, v12, v17, v8
	v_mul_f32_e32 v17, v58, v65
	v_mul_f32_e32 v18, 0xbfb8aa3b, v6
	v_mul_f32_e32 v12, 0xbfb8aa3b, v8
	v_fma_f32 v9, v13, v17, v9
	v_exp_f32_e32 v18, v18
	v_mul_f32_e32 v4, v4, v16
	v_add_f32_e32 v16, 1.0, v19
	v_exp_f32_e32 v12, v12
	v_mul_f32_e32 v13, 0xbfb8aa3b, v9
	v_rcp_f32_e32 v16, v16
	v_exp_f32_e32 v13, v13
	v_add_f32_e32 v18, 1.0, v18
	v_add_f32_e32 v12, 1.0, v12
	v_rcp_f32_e32 v18, v18
	v_mul_f32_e32 v7, v7, v16
	v_rcp_f32_e32 v12, v12
	v_add_f32_e32 v13, 1.0, v13
	v_mul_f32_e32 v16, v64, v65
	v_fma_f32 v10, v14, v16, v10
	v_mul_f32_e32 v16, v67, v65
	v_rcp_f32_e32 v13, v13
	v_fmac_f32_e32 v11, v15, v16
	v_mul_f32_e32 v14, 0xbfb8aa3b, v10
	v_mul_f32_e32 v15, 0xbfb8aa3b, v11
	v_mul_f32_e32 v6, v6, v18
	v_exp_f32_e32 v14, v14
	v_exp_f32_e32 v15, v15
	v_mul_f32_e32 v8, v8, v12
	v_mul_f32_e32 v9, v9, v13
	v_cvt_pk_bf16_f32 v4, v4, v5
	v_cvt_pk_bf16_f32 v5, v6, v7
	v_cvt_pk_bf16_f32 v6, v8, v9
	v_add_u32_e32 v8, s87, v106
	v_ashrrev_i32_e32 v9, 31, v8
	v_lshlrev_b64 v[8:9], 12, v[8:9]
	v_add_f32_e32 v14, 1.0, v14
	v_add_f32_e32 v15, 1.0, v15
	v_lshl_add_u64 v[8:9], s[6:7], 0, v[8:9]
	v_rcp_f32_e32 v14, v14
	v_rcp_f32_e32 v15, v15
	v_lshl_add_u64 v[8:9], v[8:9], 0, v[28:29]
	v_lshl_add_u64 v[8:9], v[8:9], 0, v[2:3]
	v_add_co_u32_e32 v8, vcc, 0x40e00000, v8
	v_mul_f32_e32 v10, v10, v14
	s_nop 0
	v_addc_co_u32_e32 v9, vcc, 0, v9, vcc
	v_mul_f32_e32 v11, v11, v15
	v_cvt_pk_bf16_f32 v7, v10, v11
	global_store_dwordx4 v[8:9], v[4:7], off offset:2048
	s_barrier
	s_cbranch_scc1 .LBB0_838
